# speedup vs baseline: 1.0055x; 1.0055x over previous
.LBB1_33:
	s_mov_b32 s5, 0
	v_lshl_add_u64 v[168:169], v[154:155], 0, s[4:5]
	global_load_dwordx4 v[154:157], v[168:169], off
	ds_read_b128 v[50:53], v179 offset:33792
	ds_read_b128 v[54:57], v179 offset:33824
	ds_read_b128 v[58:61], v179 offset:33856
	ds_read_b128 v[62:65], v179 offset:33888
	ds_read_b128 v[180:183], v179 offset:33920
	ds_read_b128 v[184:187], v179 offset:33952
	s_waitcnt lgkmcnt(5)
	v_mfma_f32_32x32x16_f16 v[34:49], v[122:125], v[50:53], v[2:17]
	ds_read_b128 v[190:193], v179 offset:33984
	v_cvt_pk_f16_f32 v174, v18, v19
	v_cvt_pk_f16_f32 v175, v20, v21
	s_waitcnt lgkmcnt(5)
	v_mfma_f32_32x32x16_f16 v[34:49], v[98:101], v[54:57], v[34:49]
	ds_read_b128 v[18:21], v179 offset:34016
	v_exp_f16_e64 v50, v174 clamp
	v_exp_f16_e64 v51, v175 clamp
	v_exp_f16_sdwa v50, v174 clamp dst_sel:WORD_1 dst_unused:UNUSED_PRESERVE src0_sel:WORD_1
	v_exp_f16_sdwa v51, v175 clamp dst_sel:WORD_1 dst_unused:UNUSED_PRESERVE src0_sel:WORD_1
	s_nop 0
	s_waitcnt lgkmcnt(5)
	v_mfma_f32_32x32x16_f16 v[34:49], v[114:117], v[58:61], v[34:49]
	ds_read_b128 v[194:197], v179 offset:34048
	s_movk_i32 s5, 0x3dc5
	v_mov_b32_e32 v188, 0xbdc5
	v_pk_fma_f16 v51, v51, s5, v188 op_sel_hi:[1,0,0]
	v_pk_fma_f16 v50, v50, s5, v188 op_sel_hi:[1,0,0]
	v_pk_max_f16 v51, v175, v51
	v_pk_max_f16 v50, v174, v50
	s_waitcnt lgkmcnt(5)
	v_mfma_f32_32x32x16_f16 v[34:49], v[86:89], v[62:65], v[34:49]
	ds_read_b128 v[200:203], v179 offset:34080
	v_cvt_pk_f16_f32 v52, v22, v23
	v_cvt_pk_f16_f32 v53, v24, v25
	s_waitcnt lgkmcnt(5)
	v_mfma_f32_32x32x16_f16 v[34:49], v[126:129], v[180:183], v[34:49]
	ds_read_b128 v[22:25], v179 offset:34112
	v_exp_f16_e64 v54, v52 clamp
	v_exp_f16_e64 v55, v53 clamp
	v_exp_f16_sdwa v54, v52 clamp dst_sel:WORD_1 dst_unused:UNUSED_PRESERVE src0_sel:WORD_1
	v_exp_f16_sdwa v55, v53 clamp dst_sel:WORD_1 dst_unused:UNUSED_PRESERVE src0_sel:WORD_1
	s_nop 0
	s_waitcnt lgkmcnt(5)
	v_mfma_f32_32x32x16_f16 v[34:49], v[90:93], v[184:187], v[34:49]
	ds_read_b128 v[180:183], v179 offset:34144
	v_pk_fma_f16 v55, v55, s5, v188 op_sel_hi:[1,0,0]
	v_pk_fma_f16 v54, v54, s5, v188 op_sel_hi:[1,0,0]
	v_pk_max_f16 v53, v53, v55
	v_pk_max_f16 v52, v52, v54
	s_waitcnt lgkmcnt(5)
	v_mfma_f32_32x32x16_f16 v[34:49], v[118:121], v[190:193], v[34:49]
	ds_read_b128 v[184:187], v179 offset:34176
	v_cvt_pk_f16_f32 v174, v26, v27
	v_cvt_pk_f16_f32 v175, v28, v29
	v_mfma_f32_16x16x32_f16 v[62:65], v[70:73], v[50:53], 0
	s_waitcnt lgkmcnt(5)
	v_mfma_f32_32x32x16_f16 v[34:49], v[78:81], v[18:21], v[34:49]
	ds_read_b128 v[26:29], v179 offset:34208
	v_exp_f16_e64 v190, v174 clamp
	v_exp_f16_e64 v191, v175 clamp
	v_exp_f16_sdwa v190, v174 clamp dst_sel:WORD_1 dst_unused:UNUSED_PRESERVE src0_sel:WORD_1
	v_exp_f16_sdwa v191, v175 clamp dst_sel:WORD_1 dst_unused:UNUSED_PRESERVE src0_sel:WORD_1
	s_nop 0
	s_waitcnt lgkmcnt(5)
	v_mfma_f32_32x32x16_f16 v[34:49], v[102:105], v[194:197], v[34:49]
	ds_read_b128 v[18:21], v179 offset:34240
	v_pk_fma_f16 v191, v191, s5, v188 op_sel_hi:[1,0,0]
	s_nop 0
	v_pk_max_f16 v191, v175, v191
	v_pk_fma_f16 v175, v190, s5, v188 op_sel_hi:[1,0,0]
	s_nop 0
	v_pk_max_f16 v190, v174, v175
	s_waitcnt lgkmcnt(5)
	v_mfma_f32_32x32x16_f16 v[34:49], v[74:77], v[200:203], v[34:49]
	ds_read_b128 v[194:197], v179 offset:34272
	v_cvt_pk_f16_f32 v30, v30, v31
	v_cvt_pk_f16_f32 v31, v32, v33
	s_waitcnt lgkmcnt(5)
	v_mfma_f32_32x32x16_f16 v[34:49], v[106:109], v[22:25], v[34:49]
	v_exp_f16_e64 v32, v30 clamp
	v_exp_f16_e64 v33, v31 clamp
	v_exp_f16_sdwa v32, v30 clamp dst_sel:WORD_1 dst_unused:UNUSED_PRESERVE src0_sel:WORD_1
	v_exp_f16_sdwa v33, v31 clamp dst_sel:WORD_1 dst_unused:UNUSED_PRESERVE src0_sel:WORD_1
	s_nop 0
	s_waitcnt lgkmcnt(4)
	v_mfma_f32_32x32x16_f16 v[34:49], v[82:85], v[180:183], v[34:49]
	v_pk_fma_f16 v22, v33, s5, v188 op_sel_hi:[1,0,0]
	s_nop 0
	v_pk_max_f16 v193, v31, v22
	v_pk_fma_f16 v22, v32, s5, v188 op_sel_hi:[1,0,0]
	s_nop 0
	v_pk_max_f16 v192, v30, v22
	s_waitcnt lgkmcnt(3)
	v_mfma_f32_32x32x16_f16 v[34:49], v[110:113], v[184:187], v[34:49]
	s_waitcnt vmcnt(2)
	v_pk_add_f16 v24, v158, v146
	v_pk_add_f16 v25, v159, v147
	s_nop 0
	v_pk_mul_f16 v22, v160, v148 clamp
	v_pk_mul_f16 v23, v161, v149 clamp
	v_pk_max_f16 v22, v24, v22
	v_pk_max_f16 v23, v25, v23
	ds_write_b64 v189, v[22:23]
	v_mfma_f32_16x16x32_f16 v[62:65], v[66:69], v[190:193], v[62:65]
	s_waitcnt lgkmcnt(3)
	v_mfma_f32_32x32x16_f16 v[34:49], v[94:97], v[26:29], v[34:49]
	v_pk_add_f16 v24, v158, v138
	v_pk_add_f16 v25, v159, v139
	s_nop 0
	v_pk_mul_f16 v22, v160, v140 clamp
	v_pk_mul_f16 v23, v161, v141 clamp
	v_pk_max_f16 v22, v24, v22
	v_pk_max_f16 v23, v25, v23
	ds_write_b64 v189, v[22:23] offset:528
	s_waitcnt lgkmcnt(3)
	v_mfma_f32_32x32x16_f16 v[34:49], v[134:137], v[18:21], v[34:49]
	v_pk_add_f16 v24, v158, v150
	v_pk_add_f16 v25, v159, v151
	s_nop 0
	v_pk_mul_f16 v22, v160, v152 clamp
	v_pk_mul_f16 v23, v161, v153 clamp
	v_pk_max_f16 v22, v24, v22
	v_pk_max_f16 v23, v25, v23
	ds_write_b64 v189, v[22:23] offset:1056
	s_waitcnt lgkmcnt(3)
	v_mfma_f32_32x32x16_f16 v[34:49], v[130:133], v[194:197], v[34:49]
	v_pk_add_f16 v20, v158, v142
	v_pk_add_f16 v21, v159, v143
	s_nop 0
	v_pk_mul_f16 v18, v160, v144 clamp
	v_pk_mul_f16 v19, v161, v145 clamp
	v_pk_max_f16 v18, v20, v18
	v_pk_max_f16 v19, v21, v19
	ds_write_b64 v189, v[18:19] offset:1584
	v_mov_b32_e32 v18, 0x12400
	v_lshl_add_u32 v201, v170, 2, v18
	v_mov_b32_e32 v18, 0x12408
	v_lshl_add_u32 v18, v167, 2, v18
	s_mov_b32 s5, 0x12400
	v_add3_u32 v18, v171, v172, s5
	ds_write2_b32 v201, v62, v63 offset1:1
	s_and_saveexec_b64 s[6:7], s[0:1]
	ds_write2_b32 v201, v64, v65 offset0:2 offset1:3
	s_or_b64 exec, exec, s[6:7]
	s_mov_b32 s5, 0
	v_lshl_add_u64 v[168:169], v[168:169], 0, s[4:5]
	global_load_dwordx4 v[158:161], v[168:169], off
	ds_read_b128 v[50:53], v179 offset:50688
	ds_read_b128 v[54:57], v179 offset:50720
	ds_read_b128 v[58:61], v179 offset:50752
	ds_read_b128 v[62:65], v179 offset:50784
	ds_read_b128 v[180:183], v179 offset:50816
	ds_read_b128 v[184:187], v179 offset:50848
	s_waitcnt lgkmcnt(5)
	v_mfma_f32_32x32x16_f16 v[18:33], v[122:125], v[50:53], v[2:17]
	ds_read_b128 v[190:193], v179 offset:50880
	v_cvt_pk_f16_f32 v174, v34, v35
	v_cvt_pk_f16_f32 v175, v36, v37
	s_waitcnt lgkmcnt(5)
	v_mfma_f32_32x32x16_f16 v[18:33], v[98:101], v[54:57], v[18:33]
	ds_read_b128 v[34:37], v179 offset:50912
	v_exp_f16_e64 v50, v174 clamp
	v_exp_f16_e64 v51, v175 clamp
	v_exp_f16_sdwa v50, v174 clamp dst_sel:WORD_1 dst_unused:UNUSED_PRESERVE src0_sel:WORD_1
	v_exp_f16_sdwa v51, v175 clamp dst_sel:WORD_1 dst_unused:UNUSED_PRESERVE src0_sel:WORD_1
	s_nop 0
	s_waitcnt lgkmcnt(5)
	v_mfma_f32_32x32x16_f16 v[18:33], v[114:117], v[58:61], v[18:33]
	ds_read_b128 v[194:197], v179 offset:50944
	s_movk_i32 s5, 0x3dc5
	v_mov_b32_e32 v188, 0xbdc5
	v_pk_fma_f16 v51, v51, s5, v188 op_sel_hi:[1,0,0]
	v_pk_fma_f16 v50, v50, s5, v188 op_sel_hi:[1,0,0]
	v_pk_max_f16 v51, v175, v51
	v_pk_max_f16 v50, v174, v50
	s_waitcnt lgkmcnt(5)
	v_mfma_f32_32x32x16_f16 v[18:33], v[86:89], v[62:65], v[18:33]
	ds_read_b128 v[202:205], v179 offset:50976
	v_cvt_pk_f16_f32 v52, v38, v39
	v_cvt_pk_f16_f32 v53, v40, v41
	s_waitcnt lgkmcnt(5)
	v_mfma_f32_32x32x16_f16 v[18:33], v[126:129], v[180:183], v[18:33]
	ds_read_b128 v[38:41], v179 offset:51008
	v_exp_f16_e64 v54, v52 clamp
	v_exp_f16_e64 v55, v53 clamp
	v_exp_f16_sdwa v54, v52 clamp dst_sel:WORD_1 dst_unused:UNUSED_PRESERVE src0_sel:WORD_1
	v_exp_f16_sdwa v55, v53 clamp dst_sel:WORD_1 dst_unused:UNUSED_PRESERVE src0_sel:WORD_1
	s_nop 0
	s_waitcnt lgkmcnt(5)
	v_mfma_f32_32x32x16_f16 v[18:33], v[90:93], v[184:187], v[18:33]
	ds_read_b128 v[180:183], v179 offset:51040
	v_pk_fma_f16 v55, v55, s5, v188 op_sel_hi:[1,0,0]
	v_pk_fma_f16 v54, v54, s5, v188 op_sel_hi:[1,0,0]
	v_pk_max_f16 v53, v53, v55
	v_pk_max_f16 v52, v52, v54
	s_waitcnt lgkmcnt(5)
	v_mfma_f32_32x32x16_f16 v[18:33], v[118:121], v[190:193], v[18:33]
	ds_read_b128 v[184:187], v179 offset:51072
	v_cvt_pk_f16_f32 v174, v42, v43
	v_cvt_pk_f16_f32 v175, v44, v45
	v_mfma_f32_16x16x32_f16 v[62:65], v[70:73], v[50:53], 0
	s_waitcnt lgkmcnt(5)
	v_mfma_f32_32x32x16_f16 v[18:33], v[78:81], v[34:37], v[18:33]
	ds_read_b128 v[42:45], v179 offset:51104
	v_exp_f16_e64 v190, v174 clamp
	v_exp_f16_e64 v191, v175 clamp
	v_exp_f16_sdwa v190, v174 clamp dst_sel:WORD_1 dst_unused:UNUSED_PRESERVE src0_sel:WORD_1
	v_exp_f16_sdwa v191, v175 clamp dst_sel:WORD_1 dst_unused:UNUSED_PRESERVE src0_sel:WORD_1
	s_nop 0
	s_waitcnt lgkmcnt(5)
	v_mfma_f32_32x32x16_f16 v[18:33], v[102:105], v[194:197], v[18:33]
	ds_read_b128 v[34:37], v179 offset:51136
	v_pk_fma_f16 v191, v191, s5, v188 op_sel_hi:[1,0,0]
	s_nop 0
	v_pk_max_f16 v191, v175, v191
	v_pk_fma_f16 v175, v190, s5, v188 op_sel_hi:[1,0,0]
	s_nop 0
	v_pk_max_f16 v190, v174, v175
	s_waitcnt lgkmcnt(5)
	v_mfma_f32_32x32x16_f16 v[18:33], v[74:77], v[202:205], v[18:33]
	ds_read_b128 v[194:197], v179 offset:51168
	v_cvt_pk_f16_f32 v46, v46, v47
	v_cvt_pk_f16_f32 v47, v48, v49
	s_waitcnt lgkmcnt(5)
	v_mfma_f32_32x32x16_f16 v[18:33], v[106:109], v[38:41], v[18:33]
	v_exp_f16_e64 v48, v46 clamp
	v_exp_f16_e64 v49, v47 clamp
	v_exp_f16_sdwa v48, v46 clamp dst_sel:WORD_1 dst_unused:UNUSED_PRESERVE src0_sel:WORD_1
	v_exp_f16_sdwa v49, v47 clamp dst_sel:WORD_1 dst_unused:UNUSED_PRESERVE src0_sel:WORD_1
	s_nop 0
	s_waitcnt lgkmcnt(4)
	v_mfma_f32_32x32x16_f16 v[18:33], v[82:85], v[180:183], v[18:33]
	v_pk_fma_f16 v38, v49, s5, v188 op_sel_hi:[1,0,0]
	s_nop 0
	v_pk_max_f16 v193, v47, v38
	v_pk_fma_f16 v38, v48, s5, v188 op_sel_hi:[1,0,0]
	s_nop 0
	v_pk_max_f16 v192, v46, v38
	s_waitcnt lgkmcnt(3)
	v_mfma_f32_32x32x16_f16 v[18:33], v[110:113], v[184:187], v[18:33]
	s_waitcnt vmcnt(2)
	v_pk_add_f16 v40, v162, v146
	v_pk_add_f16 v41, v163, v147
	s_nop 0
	v_pk_mul_f16 v38, v164, v148 clamp
	v_pk_mul_f16 v39, v165, v149 clamp
	v_pk_max_f16 v38, v40, v38
	v_pk_max_f16 v39, v41, v39
	ds_write_b64 v189, v[38:39] offset:16896
	v_mfma_f32_16x16x32_f16 v[62:65], v[66:69], v[190:193], v[62:65]
	s_waitcnt lgkmcnt(3)
	v_mfma_f32_32x32x16_f16 v[18:33], v[94:97], v[42:45], v[18:33]
	v_pk_add_f16 v40, v162, v138
	v_pk_add_f16 v41, v163, v139
	s_nop 0
	v_pk_mul_f16 v38, v164, v140 clamp
	v_pk_mul_f16 v39, v165, v141 clamp
	v_pk_max_f16 v38, v40, v38
	v_pk_max_f16 v39, v41, v39
	ds_write_b64 v189, v[38:39] offset:17424
	s_waitcnt lgkmcnt(3)
	v_mfma_f32_32x32x16_f16 v[18:33], v[134:137], v[34:37], v[18:33]
	v_pk_add_f16 v40, v162, v150
	v_pk_add_f16 v41, v163, v151
	s_nop 0
	v_pk_mul_f16 v38, v164, v152 clamp
	v_pk_mul_f16 v39, v165, v153 clamp
	v_pk_max_f16 v38, v40, v38
	v_pk_max_f16 v39, v41, v39
	ds_write_b64 v189, v[38:39] offset:17952
	s_waitcnt lgkmcnt(3)
	v_mfma_f32_32x32x16_f16 v[18:33], v[130:133], v[194:197], v[18:33]
	v_pk_add_f16 v36, v162, v142
	v_pk_add_f16 v37, v163, v143
	s_nop 0
	v_pk_mul_f16 v34, v164, v144 clamp
	v_pk_mul_f16 v35, v165, v145 clamp
	v_pk_max_f16 v34, v36, v34
	v_pk_max_f16 v35, v37, v35
	ds_write_b64 v189, v[34:35] offset:18480
	v_mov_b32_e32 v34, 0x14000
	v_lshl_add_u32 v211, v170, 2, v34
	v_mov_b32_e32 v34, 0x14008
	v_lshl_add_u32 v34, v167, 2, v34
	s_mov_b32 s5, 0x14000
	v_add3_u32 v34, v171, v172, s5
	ds_write2_b32 v211, v62, v63 offset1:1
	s_and_saveexec_b64 s[6:7], s[0:1]
	ds_write2_b32 v211, v64, v65 offset0:2 offset1:3
	s_or_b64 exec, exec, s[6:7]
	s_mov_b32 s21, 0
	s_mov_b32 s5, s21
	v_lshl_add_u64 v[168:169], v[168:169], 0, s[4:5]
	s_sub_i32 s4, 0x7e, s28
	s_mul_i32 s4, s4, 6
	s_ashr_i32 s5, s4, 31
	s_add_u32 s26, s8, s4
	s_addc_u32 s27, s9, s5
	s_or_b32 s31, s28, 1
	s_or_b64 s[4:5], s[18:19], s[22:23]
	s_and_b64 s[4:5], s[4:5], exec
	s_cselect_b32 s6, s13, s46
	s_cselect_b32 s7, s12, s45
	s_lshl_b32 s4, s30, 6
	s_ashr_i32 s5, s4, 31
	s_lshl_b64 s[4:5], s[4:5], 4
	s_add_u32 s4, s7, s4
	s_addc_u32 s5, s6, s5
	s_lshl_b32 s51, s29, 4
	s_sub_i32 s9, 0xff, s51
	s_mul_i32 s9, s9, s51
	s_sub_i32 s28, s43, s29
	s_ashr_i32 s9, s9, 1
	s_lshl_b32 s28, s28, 4
	s_add_i32 s9, s28, s9
	s_add_i32 s9, s9, -1
	s_mul_i32 s8, s33, 0x1fc0
	s_ashr_i32 s28, s9, 31
	v_mov_b32_e32 v167, 0
	v_lshlrev_b32_e32 v34, 2, v173
	s_add_u32 s8, s9, s8
	v_lshl_add_u64 v[174:175], s[4:5], 0, v[166:167]
	v_cndmask_b32_e64 v231, 0, 1, s[16:17]
	s_movk_i32 s4, 0xc0
	v_add_u32_e32 v200, 0x12400, v34
	s_addc_u32 s9, s28, 0
	v_add_u32_e32 v190, 0x14000, v34
	v_add_u32_e32 v180, 0x15c00, v34
	v_add_u32_e32 v216, 0x10800, v34
	v_add_u32_e32 v209, 0x125c0, v34
	v_add_u32_e32 v210, 0x12940, v34
	v_add_u32_e32 v207, 0x12cc0, v34
	v_add_u32_e32 v208, 0x13040, v34
	v_add_u32_e32 v204, 0x133c0, v34
	v_add_u32_e32 v205, 0x13740, v34
	v_add_u32_e32 v202, 0x13ac0, v34
	v_add_u32_e32 v203, 0x13e40, v34
	v_add_u32_e32 v197, 0x141c0, v34
	v_add_u32_e32 v198, 0x14540, v34
	v_add_u32_e32 v195, 0x148c0, v34
	v_add_u32_e32 v196, 0x14c40, v34
	v_add_u32_e32 v193, 0x14fc0, v34
	v_add_u32_e32 v194, 0x15340, v34
	v_add_u32_e32 v191, 0x156c0, v34
	v_add_u32_e32 v192, 0x15a40, v34
	v_add_u32_e32 v187, 0x15dc0, v34
	v_add_u32_e32 v188, 0x16140, v34
	v_add_u32_e32 v185, 0x164c0, v34
	v_add_u32_e32 v186, 0x16840, v34
	v_add_u32_e32 v183, 0x16bc0, v34
	v_add_u32_e32 v184, 0x16f40, v34
	v_add_u32_e32 v181, 0x172c0, v34
	v_add_u32_e32 v182, 0x17640, v34
	v_add_u32_e32 v223, 0x109c0, v34
	v_add_u32_e32 v224, 0x10d40, v34
	v_add_u32_e32 v221, 0x110c0, v34
	v_add_u32_e32 v222, 0x11440, v34
	v_add_u32_e32 v219, 0x117c0, v34
	v_add_u32_e32 v220, 0x11b40, v34
	v_add_u32_e32 v217, 0x11ec0, v34
	v_add_u32_e32 v218, 0x12240, v34
	v_mov_b32_e32 v34, 0x17800
	v_cndmask_b32_e64 v230, 0, 1, s[18:19]
	v_readfirstlane_b32 s50, v231
	v_cmp_gt_u32_e64 s[6:7], s4, v0
	s_movk_i32 s4, 0x60
	s_mul_i32 s9, s9, 6
	s_mul_hi_u32 s28, s8, 6
	v_mov_b32_e32 v35, 0x15c00
	v_add_u32_e32 v228, 0x15c00, v171
	v_add_u32_e32 v226, 0x10800, v171
	v_add_u32_e32 v215, 0x12400, v171
	v_add_u32_e32 v213, 0x14000, v171
	v_lshl_add_u32 v232, v177, 2, v34
	v_cndmask_b32_e64 v34, 0, 1, s[24:25]
	s_mov_b32 s48, 1
	v_readfirstlane_b32 s49, v230
	v_cmp_gt_u32_e64 s[4:5], s4, v0
	s_add_i32 s52, s28, s9
	s_mul_i32 s53, s8, 6
	v_lshl_add_u32 v229, v170, 2, v35
	v_add_u32_e32 v227, v228, v172
	v_add_u32_e32 v225, v226, v172
	v_add_u32_e32 v214, v215, v172
	v_add_u32_e32 v212, v213, v172
	s_mov_b32 s56, 8
	s_mov_b32 s54, 16
	v_cmp_ne_u32_e64 s[8:9], 1, v34
	s_movk_i32 s55, 0x3dc5
	v_mov_b32_e32 v233, 0xbdc5
	v_add_u32_e32 v234, 0x700, v200
	v_add_u32_e32 v235, 0xe00, v200
	v_add_u32_e32 v236, 0x1500, v200
	v_add_u32_e32 v237, 0x700, v190
	v_add_u32_e32 v238, 0xe00, v190
	v_add_u32_e32 v239, 0x1500, v190
	s_mov_b32 s41, s50
	s_waitcnt lgkmcnt(0)
	s_barrier
	ds_read_b128 v[50:53], v179
	ds_read_b128 v[54:57], v179 offset:32
	s_and_b64 vcc, exec, s[8:9]
	s_cbranch_vccnz .LBB1_50

.LBB1_59:
	global_load_dwordx4 v[162:165], v[168:169], off
	ds_read_b128 v[58:61], v179 offset:64
	ds_read_b128 v[62:65], v179 offset:96
	ds_read_b128 v[170:173], v179 offset:128
	ds_read_b128 v[240:243], v179 offset:160
	s_waitcnt lgkmcnt(5)
	v_mfma_f32_32x32x16_f16 v[34:49], v[122:125], v[50:53], v[2:17]
	ds_read_b128 v[244:247], v179 offset:192
	v_cvt_pk_f16_f32 v166, v18, v19
	v_cvt_pk_f16_f32 v167, v20, v21
	s_waitcnt lgkmcnt(5)
	v_mfma_f32_32x32x16_f16 v[34:49], v[98:101], v[54:57], v[34:49]
	ds_read_b128 v[18:21], v179 offset:224
	v_exp_f16_e64 v50, v166 clamp
	v_exp_f16_e64 v51, v167 clamp
	v_exp_f16_sdwa v50, v166 clamp dst_sel:WORD_1 dst_unused:UNUSED_PRESERVE src0_sel:WORD_1
	v_exp_f16_sdwa v51, v167 clamp dst_sel:WORD_1 dst_unused:UNUSED_PRESERVE src0_sel:WORD_1
	s_nop 0
	s_waitcnt lgkmcnt(5)
	v_mfma_f32_32x32x16_f16 v[34:49], v[114:117], v[58:61], v[34:49]
	ds_read_b128 v[248:251], v179 offset:256
	v_pk_fma_f16 v51, v51, s55, v233 op_sel_hi:[1,0,0]
	v_pk_fma_f16 v50, v50, s55, v233 op_sel_hi:[1,0,0]
	v_pk_max_f16 v51, v167, v51
	v_pk_max_f16 v50, v166, v50
	s_waitcnt lgkmcnt(5)
	v_mfma_f32_32x32x16_f16 v[34:49], v[86:89], v[62:65], v[34:49]
	ds_read_b128 v[252:255], v179 offset:288
	v_cvt_pk_f16_f32 v52, v22, v23
	v_cvt_pk_f16_f32 v53, v24, v25
	s_waitcnt lgkmcnt(5)
	v_mfma_f32_32x32x16_f16 v[34:49], v[126:129], v[170:173], v[34:49]
	ds_read_b128 v[22:25], v179 offset:320
	v_exp_f16_e64 v54, v52 clamp
	v_exp_f16_e64 v55, v53 clamp
	v_exp_f16_sdwa v54, v52 clamp dst_sel:WORD_1 dst_unused:UNUSED_PRESERVE src0_sel:WORD_1
	v_exp_f16_sdwa v55, v53 clamp dst_sel:WORD_1 dst_unused:UNUSED_PRESERVE src0_sel:WORD_1
	s_nop 0
	s_waitcnt lgkmcnt(5)
	v_mfma_f32_32x32x16_f16 v[34:49], v[90:93], v[240:243], v[34:49]
	ds_read_b128 v[170:173], v179 offset:352
	v_pk_fma_f16 v55, v55, s55, v233 op_sel_hi:[1,0,0]
	v_pk_fma_f16 v54, v54, s55, v233 op_sel_hi:[1,0,0]
	v_pk_max_f16 v53, v53, v55
	v_pk_max_f16 v52, v52, v54
	s_waitcnt lgkmcnt(5)
	v_mfma_f32_32x32x16_f16 v[34:49], v[118:121], v[244:247], v[34:49]
	ds_read_b128 v[240:243], v179 offset:384
	v_cvt_pk_f16_f32 v166, v26, v27
	v_cvt_pk_f16_f32 v167, v28, v29
	v_mfma_f32_16x16x32_f16 v[62:65], v[70:73], v[50:53], 0
	s_waitcnt lgkmcnt(5)
	v_mfma_f32_32x32x16_f16 v[34:49], v[78:81], v[18:21], v[34:49]
	ds_read_b128 v[26:29], v179 offset:416
	v_exp_f16_e64 v244, v166 clamp
	v_exp_f16_e64 v245, v167 clamp
	v_exp_f16_sdwa v244, v166 clamp dst_sel:WORD_1 dst_unused:UNUSED_PRESERVE src0_sel:WORD_1
	v_exp_f16_sdwa v245, v167 clamp dst_sel:WORD_1 dst_unused:UNUSED_PRESERVE src0_sel:WORD_1
	s_nop 0
	s_waitcnt lgkmcnt(5)
	v_mfma_f32_32x32x16_f16 v[34:49], v[102:105], v[248:251], v[34:49]
	ds_read_b128 v[18:21], v179 offset:448
	v_pk_fma_f16 v245, v245, s55, v233 op_sel_hi:[1,0,0]
	s_nop 0
	v_pk_max_f16 v245, v167, v245
	v_pk_fma_f16 v167, v244, s55, v233 op_sel_hi:[1,0,0]
	s_nop 0
	v_pk_max_f16 v244, v166, v167
	s_waitcnt lgkmcnt(5)
	v_mfma_f32_32x32x16_f16 v[34:49], v[74:77], v[252:255], v[34:49]
	ds_read_b128 v[248:251], v179 offset:480
	v_cvt_pk_f16_f32 v30, v30, v31
	v_cvt_pk_f16_f32 v31, v32, v33
	s_waitcnt lgkmcnt(5)
	v_mfma_f32_32x32x16_f16 v[34:49], v[106:109], v[22:25], v[34:49]
	v_exp_f16_e64 v32, v30 clamp
	v_exp_f16_e64 v33, v31 clamp
	v_exp_f16_sdwa v32, v30 clamp dst_sel:WORD_1 dst_unused:UNUSED_PRESERVE src0_sel:WORD_1
	v_exp_f16_sdwa v33, v31 clamp dst_sel:WORD_1 dst_unused:UNUSED_PRESERVE src0_sel:WORD_1
	s_nop 0
	s_waitcnt lgkmcnt(4)
	v_mfma_f32_32x32x16_f16 v[34:49], v[82:85], v[170:173], v[34:49]
	v_pk_fma_f16 v22, v33, s55, v233 op_sel_hi:[1,0,0]
	s_nop 0
	v_pk_max_f16 v247, v31, v22
	v_pk_fma_f16 v22, v32, s55, v233 op_sel_hi:[1,0,0]
	s_nop 0
	v_pk_max_f16 v246, v30, v22
	s_waitcnt lgkmcnt(3)
	v_mfma_f32_32x32x16_f16 v[34:49], v[110:113], v[240:243], v[34:49]
	s_waitcnt vmcnt(2)
	v_pk_add_f16 v24, v154, v146
	v_pk_add_f16 v25, v155, v147
	s_nop 0
	v_pk_mul_f16 v22, v156, v148 clamp
	v_pk_mul_f16 v23, v157, v149 clamp
	v_pk_max_f16 v22, v24, v22
	v_pk_max_f16 v23, v25, v23
	ds_write_b64 v189, v[22:23] offset:33792
	v_mfma_f32_16x16x32_f16 v[62:65], v[66:69], v[244:247], v[62:65]
	s_waitcnt lgkmcnt(3)
	v_mfma_f32_32x32x16_f16 v[34:49], v[94:97], v[26:29], v[34:49]
	v_pk_add_f16 v24, v154, v138
	v_pk_add_f16 v25, v155, v139
	s_nop 0
	v_pk_mul_f16 v22, v156, v140 clamp
	v_pk_mul_f16 v23, v157, v141 clamp
	v_pk_max_f16 v22, v24, v22
	v_pk_max_f16 v23, v25, v23
	ds_write_b64 v189, v[22:23] offset:34320
	s_waitcnt lgkmcnt(3)
	v_mfma_f32_32x32x16_f16 v[34:49], v[134:137], v[18:21], v[34:49]
	v_pk_add_f16 v24, v154, v150
	v_pk_add_f16 v25, v155, v151
	s_nop 0
	v_pk_mul_f16 v22, v156, v152 clamp
	v_pk_mul_f16 v23, v157, v153 clamp
	v_pk_max_f16 v22, v24, v22
	v_pk_max_f16 v23, v25, v23
	ds_write_b64 v189, v[22:23] offset:34848
	s_waitcnt lgkmcnt(3)
	v_mfma_f32_32x32x16_f16 v[34:49], v[130:133], v[248:251], v[34:49]
	v_pk_add_f16 v20, v154, v142
	v_pk_add_f16 v21, v155, v143
	s_nop 0
	v_pk_mul_f16 v18, v156, v144 clamp
	v_pk_mul_f16 v19, v157, v145 clamp
	v_pk_max_f16 v18, v20, v18
	v_pk_max_f16 v19, v21, v19
	ds_write_b64 v189, v[18:19] offset:35376
	ds_write2_b32 v229, v62, v63 offset1:1
	s_and_saveexec_b64 s[28:29], s[0:1]
	ds_write2_b32 v229, v64, v65 offset0:2 offset1:3
	s_or_b64 exec, exec, s[28:29]
	v_lshl_add_u64 v[166:167], s[20:21], 4, v[168:169]
	global_load_dwordx4 v[154:157], v[166:167], off
	ds_read_b128 v[50:53], v179 offset:16896
	ds_read_b128 v[54:57], v179 offset:16928
	ds_read_b128 v[58:61], v179 offset:16960
	ds_read_b128 v[62:65], v179 offset:16992
	ds_read_b128 v[168:171], v179 offset:17024
	ds_read_b128 v[240:243], v179 offset:17056
	s_waitcnt lgkmcnt(5)
	v_mfma_f32_32x32x16_f16 v[18:33], v[122:125], v[50:53], v[2:17]
	ds_read_b128 v[244:247], v179 offset:17088
	v_cvt_pk_f16_f32 v172, v34, v35
	v_cvt_pk_f16_f32 v173, v36, v37
	s_waitcnt lgkmcnt(5)
	v_mfma_f32_32x32x16_f16 v[18:33], v[98:101], v[54:57], v[18:33]
	ds_read_b128 v[34:37], v179 offset:17120
	v_exp_f16_e64 v50, v172 clamp
	v_exp_f16_e64 v51, v173 clamp
	v_exp_f16_sdwa v50, v172 clamp dst_sel:WORD_1 dst_unused:UNUSED_PRESERVE src0_sel:WORD_1
	v_exp_f16_sdwa v51, v173 clamp dst_sel:WORD_1 dst_unused:UNUSED_PRESERVE src0_sel:WORD_1
	s_nop 0
	s_waitcnt lgkmcnt(5)
	v_mfma_f32_32x32x16_f16 v[18:33], v[114:117], v[58:61], v[18:33]
	ds_read_b128 v[248:251], v179 offset:17152
	v_pk_fma_f16 v51, v51, s55, v233 op_sel_hi:[1,0,0]
	v_pk_fma_f16 v50, v50, s55, v233 op_sel_hi:[1,0,0]
	v_pk_max_f16 v51, v173, v51
	v_pk_max_f16 v50, v172, v50
	s_waitcnt lgkmcnt(5)
	v_mfma_f32_32x32x16_f16 v[18:33], v[86:89], v[62:65], v[18:33]
	ds_read_b128 v[252:255], v179 offset:17184
	v_cvt_pk_f16_f32 v52, v38, v39
	v_cvt_pk_f16_f32 v53, v40, v41
	s_waitcnt lgkmcnt(5)
	v_mfma_f32_32x32x16_f16 v[18:33], v[126:129], v[168:171], v[18:33]
	ds_read_b128 v[38:41], v179 offset:17216
	v_exp_f16_e64 v54, v52 clamp
	v_exp_f16_e64 v55, v53 clamp
	v_exp_f16_sdwa v54, v52 clamp dst_sel:WORD_1 dst_unused:UNUSED_PRESERVE src0_sel:WORD_1
	v_exp_f16_sdwa v55, v53 clamp dst_sel:WORD_1 dst_unused:UNUSED_PRESERVE src0_sel:WORD_1
	s_nop 0
	s_waitcnt lgkmcnt(5)
	v_mfma_f32_32x32x16_f16 v[18:33], v[90:93], v[240:243], v[18:33]
	ds_read_b128 v[168:171], v179 offset:17248
	v_pk_fma_f16 v55, v55, s55, v233 op_sel_hi:[1,0,0]
	v_pk_fma_f16 v54, v54, s55, v233 op_sel_hi:[1,0,0]
	v_pk_max_f16 v53, v53, v55
	v_pk_max_f16 v52, v52, v54
	s_waitcnt lgkmcnt(5)
	v_mfma_f32_32x32x16_f16 v[18:33], v[118:121], v[244:247], v[18:33]
	ds_read_b128 v[240:243], v179 offset:17280
	v_cvt_pk_f16_f32 v172, v42, v43
	v_cvt_pk_f16_f32 v173, v44, v45
	v_mfma_f32_16x16x32_f16 v[62:65], v[70:73], v[50:53], 0
	s_waitcnt lgkmcnt(5)
	v_mfma_f32_32x32x16_f16 v[18:33], v[78:81], v[34:37], v[18:33]
	ds_read_b128 v[42:45], v179 offset:17312
	v_exp_f16_e64 v244, v172 clamp
	v_exp_f16_e64 v245, v173 clamp
	v_exp_f16_sdwa v244, v172 clamp dst_sel:WORD_1 dst_unused:UNUSED_PRESERVE src0_sel:WORD_1
	v_exp_f16_sdwa v245, v173 clamp dst_sel:WORD_1 dst_unused:UNUSED_PRESERVE src0_sel:WORD_1
	s_nop 0
	s_waitcnt lgkmcnt(5)
	v_mfma_f32_32x32x16_f16 v[18:33], v[102:105], v[248:251], v[18:33]
	ds_read_b128 v[34:37], v179 offset:17344
	v_pk_fma_f16 v245, v245, s55, v233 op_sel_hi:[1,0,0]
	s_nop 0
	v_pk_max_f16 v245, v173, v245
	v_pk_fma_f16 v173, v244, s55, v233 op_sel_hi:[1,0,0]
	s_nop 0
	v_pk_max_f16 v244, v172, v173
	s_waitcnt lgkmcnt(5)
	v_mfma_f32_32x32x16_f16 v[18:33], v[74:77], v[252:255], v[18:33]
	ds_read_b128 v[248:251], v179 offset:17376
	v_cvt_pk_f16_f32 v46, v46, v47
	v_cvt_pk_f16_f32 v47, v48, v49
	s_waitcnt lgkmcnt(5)
	v_mfma_f32_32x32x16_f16 v[18:33], v[106:109], v[38:41], v[18:33]
	v_exp_f16_e64 v48, v46 clamp
	v_exp_f16_e64 v49, v47 clamp
	v_exp_f16_sdwa v48, v46 clamp dst_sel:WORD_1 dst_unused:UNUSED_PRESERVE src0_sel:WORD_1
	v_exp_f16_sdwa v49, v47 clamp dst_sel:WORD_1 dst_unused:UNUSED_PRESERVE src0_sel:WORD_1
	s_nop 0
	s_waitcnt lgkmcnt(4)
	v_mfma_f32_32x32x16_f16 v[18:33], v[82:85], v[168:171], v[18:33]
	v_pk_fma_f16 v38, v49, s55, v233 op_sel_hi:[1,0,0]
	s_nop 0
	v_pk_max_f16 v247, v47, v38
	v_pk_fma_f16 v38, v48, s55, v233 op_sel_hi:[1,0,0]
	s_nop 0
	v_pk_max_f16 v246, v46, v38
	s_waitcnt lgkmcnt(3)
	v_mfma_f32_32x32x16_f16 v[18:33], v[110:113], v[240:243], v[18:33]
	s_waitcnt vmcnt(2)
	v_pk_add_f16 v40, v158, v146
	v_pk_add_f16 v41, v159, v147
	s_nop 0
	v_pk_mul_f16 v38, v160, v148 clamp
	v_pk_mul_f16 v39, v161, v149 clamp
	v_pk_max_f16 v38, v40, v38
	v_pk_max_f16 v39, v41, v39
	ds_write_b64 v189, v[38:39] offset:50688
	v_mfma_f32_16x16x32_f16 v[62:65], v[66:69], v[244:247], v[62:65]
	s_waitcnt lgkmcnt(3)
	v_mfma_f32_32x32x16_f16 v[18:33], v[94:97], v[42:45], v[18:33]
	v_pk_add_f16 v40, v158, v138
	v_pk_add_f16 v41, v159, v139
	s_nop 0
	v_pk_mul_f16 v38, v160, v140 clamp
	v_pk_mul_f16 v39, v161, v141 clamp
	v_pk_max_f16 v38, v40, v38
	v_pk_max_f16 v39, v41, v39
	ds_write_b64 v189, v[38:39] offset:51216
	s_waitcnt lgkmcnt(3)
	v_mfma_f32_32x32x16_f16 v[18:33], v[134:137], v[34:37], v[18:33]
	v_pk_add_f16 v40, v158, v150
	v_pk_add_f16 v41, v159, v151
	s_nop 0
	v_pk_mul_f16 v38, v160, v152 clamp
	v_pk_mul_f16 v39, v161, v153 clamp
	v_pk_max_f16 v38, v40, v38
	v_pk_max_f16 v39, v41, v39
	ds_write_b64 v189, v[38:39] offset:51744
	s_waitcnt lgkmcnt(3)
	v_mfma_f32_32x32x16_f16 v[18:33], v[130:133], v[248:251], v[18:33]
	v_pk_add_f16 v36, v158, v142
	v_pk_add_f16 v37, v159, v143
	s_nop 0
	v_pk_mul_f16 v34, v160, v144 clamp
	v_pk_mul_f16 v35, v161, v145 clamp
	v_pk_max_f16 v34, v36, v34
	v_pk_max_f16 v35, v37, v35
	ds_write_b64 v189, v[34:35] offset:52272
	ds_write2_b32 v206, v62, v63 offset1:1
	s_and_saveexec_b64 s[28:29], s[0:1]
	ds_write2_b32 v206, v64, v65 offset0:2 offset1:3
	s_or_b64 exec, exec, s[28:29]
	s_sub_i32 s28, 0x7d, s31
	s_mul_i32 s28, s28, 6
	s_ashr_i32 s29, s28, 31
	s_add_u32 s26, s26, s28
	s_addc_u32 s27, s27, s29
	s_and_b64 vcc, exec, s[8:9]
	s_waitcnt lgkmcnt(0)
	s_barrier
	ds_read_b128 v[50:53], v179 offset:33792
	ds_read_b128 v[54:57], v179 offset:33824
	s_cbranch_vccnz .LBB1_76
	s_cmp_lg_u32 s41, 0
	s_cbranch_scc0 .LBB1_72
	s_and_saveexec_b64 s[28:29], s[6:7]
	s_cbranch_execz .LBB1_71
	ds_read2_b32 v[34:35], v180 offset1:224
	v_add_u32_e32 v36, 0x700, v180
	ds_read2_b32 v[36:37], v36 offset1:224
	v_add_u32_e32 v38, 0xe00, v180
	s_lshl_b32 s30, s56, 28
	s_waitcnt lgkmcnt(1)
	v_add_f32_e32 v34, 0, v34
	v_add_f32_e32 v40, v34, v35
	ds_read2_b32 v[34:35], v38 offset1:224
	v_add_u32_e32 v38, 0x1500, v180
	ds_read2_b32 v[38:39], v38 offset1:224
	s_waitcnt lgkmcnt(2)
	v_add_f32_e32 v36, v40, v36
	v_add_f32_e32 v36, v36, v37
	s_waitcnt lgkmcnt(1)
	v_add_f32_e32 v34, v36, v34
	s_add_i32 s30, s30, 0xb0000000
	v_add_f32_e32 v34, v34, v35
	s_ashr_i32 s30, s30, 31
	s_waitcnt lgkmcnt(0)
	v_add_f32_e32 v34, v34, v38
	s_and_b32 s30, s30, 0x1800
	v_add_f32_e32 v34, v34, v39
	v_add_u32_e32 v35, s30, v232
	ds_write_b32 v35, v34 offset:384

.LBB1_93:
	v_lshl_add_u64 v[158:159], s[20:21], 4, v[166:167]
	global_load_dwordx4 v[170:173], v[158:159], off
	ds_read_b128 v[58:61], v179 offset:33856
	ds_read_b128 v[62:65], v179 offset:33888
	ds_read_b128 v[166:169], v179 offset:33920
	ds_read_b128 v[240:243], v179 offset:33952
	s_add_i32 s34, s57, 1
	s_waitcnt lgkmcnt(5)
	v_mfma_f32_32x32x16_f16 v[34:49], v[122:125], v[50:53], v[2:17]
	ds_read_b128 v[244:247], v179 offset:33984
	v_cvt_pk_f16_f32 v160, v18, v19
	v_cvt_pk_f16_f32 v161, v20, v21
	s_waitcnt lgkmcnt(5)
	v_mfma_f32_32x32x16_f16 v[34:49], v[98:101], v[54:57], v[34:49]
	ds_read_b128 v[18:21], v179 offset:34016
	v_exp_f16_e64 v50, v160 clamp
	v_exp_f16_e64 v51, v161 clamp
	v_exp_f16_sdwa v50, v160 clamp dst_sel:WORD_1 dst_unused:UNUSED_PRESERVE src0_sel:WORD_1
	v_exp_f16_sdwa v51, v161 clamp dst_sel:WORD_1 dst_unused:UNUSED_PRESERVE src0_sel:WORD_1
	s_nop 0
	s_waitcnt lgkmcnt(5)
	v_mfma_f32_32x32x16_f16 v[34:49], v[114:117], v[58:61], v[34:49]
	ds_read_b128 v[248:251], v179 offset:34048
	v_pk_fma_f16 v51, v51, s55, v233 op_sel_hi:[1,0,0]
	v_pk_fma_f16 v50, v50, s55, v233 op_sel_hi:[1,0,0]
	v_pk_max_f16 v51, v161, v51
	v_pk_max_f16 v50, v160, v50
	s_waitcnt lgkmcnt(5)
	v_mfma_f32_32x32x16_f16 v[34:49], v[86:89], v[62:65], v[34:49]
	ds_read_b128 v[252:255], v179 offset:34080
	v_cvt_pk_f16_f32 v52, v22, v23
	v_cvt_pk_f16_f32 v53, v24, v25
	s_waitcnt lgkmcnt(5)
	v_mfma_f32_32x32x16_f16 v[34:49], v[126:129], v[166:169], v[34:49]
	ds_read_b128 v[22:25], v179 offset:34112
	v_exp_f16_e64 v54, v52 clamp
	v_exp_f16_e64 v55, v53 clamp
	v_exp_f16_sdwa v54, v52 clamp dst_sel:WORD_1 dst_unused:UNUSED_PRESERVE src0_sel:WORD_1
	v_exp_f16_sdwa v55, v53 clamp dst_sel:WORD_1 dst_unused:UNUSED_PRESERVE src0_sel:WORD_1
	s_nop 0
	s_waitcnt lgkmcnt(5)
	v_mfma_f32_32x32x16_f16 v[34:49], v[90:93], v[240:243], v[34:49]
	ds_read_b128 v[166:169], v179 offset:34144
	v_pk_fma_f16 v55, v55, s55, v233 op_sel_hi:[1,0,0]
	v_pk_fma_f16 v54, v54, s55, v233 op_sel_hi:[1,0,0]
	v_pk_max_f16 v53, v53, v55
	v_pk_max_f16 v52, v52, v54
	s_waitcnt lgkmcnt(5)
	v_mfma_f32_32x32x16_f16 v[34:49], v[118:121], v[244:247], v[34:49]
	ds_read_b128 v[240:243], v179 offset:34176
	v_cvt_pk_f16_f32 v160, v26, v27
	v_cvt_pk_f16_f32 v161, v28, v29
	v_mfma_f32_16x16x32_f16 v[62:65], v[70:73], v[50:53], 0
	s_waitcnt lgkmcnt(5)
	v_mfma_f32_32x32x16_f16 v[34:49], v[78:81], v[18:21], v[34:49]
	ds_read_b128 v[26:29], v179 offset:34208
	v_exp_f16_e64 v244, v160 clamp
	v_exp_f16_e64 v245, v161 clamp
	v_exp_f16_sdwa v244, v160 clamp dst_sel:WORD_1 dst_unused:UNUSED_PRESERVE src0_sel:WORD_1
	v_exp_f16_sdwa v245, v161 clamp dst_sel:WORD_1 dst_unused:UNUSED_PRESERVE src0_sel:WORD_1
	s_nop 0
	s_waitcnt lgkmcnt(5)
	v_mfma_f32_32x32x16_f16 v[34:49], v[102:105], v[248:251], v[34:49]
	ds_read_b128 v[18:21], v179 offset:34240
	v_pk_fma_f16 v245, v245, s55, v233 op_sel_hi:[1,0,0]
	s_nop 0
	v_pk_max_f16 v245, v161, v245
	v_pk_fma_f16 v161, v244, s55, v233 op_sel_hi:[1,0,0]
	s_nop 0
	v_pk_max_f16 v244, v160, v161
	s_waitcnt lgkmcnt(5)
	v_mfma_f32_32x32x16_f16 v[34:49], v[74:77], v[252:255], v[34:49]
	ds_read_b128 v[248:251], v179 offset:34272
	v_cvt_pk_f16_f32 v30, v30, v31
	v_cvt_pk_f16_f32 v31, v32, v33
	s_waitcnt lgkmcnt(5)
	v_mfma_f32_32x32x16_f16 v[34:49], v[106:109], v[22:25], v[34:49]
	v_exp_f16_e64 v32, v30 clamp
	v_exp_f16_e64 v33, v31 clamp
	v_exp_f16_sdwa v32, v30 clamp dst_sel:WORD_1 dst_unused:UNUSED_PRESERVE src0_sel:WORD_1
	v_exp_f16_sdwa v33, v31 clamp dst_sel:WORD_1 dst_unused:UNUSED_PRESERVE src0_sel:WORD_1
	s_nop 0
	s_waitcnt lgkmcnt(4)
	v_mfma_f32_32x32x16_f16 v[34:49], v[82:85], v[166:169], v[34:49]
	v_pk_fma_f16 v22, v33, s55, v233 op_sel_hi:[1,0,0]
	s_nop 0
	v_pk_max_f16 v247, v31, v22
	v_pk_fma_f16 v22, v32, s55, v233 op_sel_hi:[1,0,0]
	s_nop 0
	v_pk_max_f16 v246, v30, v22
	s_waitcnt lgkmcnt(3)
	v_mfma_f32_32x32x16_f16 v[34:49], v[110:113], v[240:243], v[34:49]
	s_waitcnt vmcnt(2)
	v_pk_add_f16 v24, v146, v162
	v_pk_add_f16 v25, v147, v163
	s_nop 0
	v_pk_mul_f16 v22, v164, v148 clamp
	v_pk_mul_f16 v23, v165, v149 clamp
	v_pk_max_f16 v22, v24, v22
	v_pk_max_f16 v23, v25, v23
	ds_write_b64 v189, v[22:23]
	v_mfma_f32_16x16x32_f16 v[62:65], v[66:69], v[244:247], v[62:65]
	s_waitcnt lgkmcnt(3)
	v_mfma_f32_32x32x16_f16 v[34:49], v[94:97], v[26:29], v[34:49]
	v_pk_add_f16 v24, v138, v162
	v_pk_add_f16 v25, v139, v163
	s_nop 0
	v_pk_mul_f16 v22, v164, v140 clamp
	v_pk_mul_f16 v23, v165, v141 clamp
	v_pk_max_f16 v22, v24, v22
	v_pk_max_f16 v23, v25, v23
	ds_write_b64 v189, v[22:23] offset:528
	s_waitcnt lgkmcnt(3)
	v_mfma_f32_32x32x16_f16 v[34:49], v[134:137], v[18:21], v[34:49]
	v_pk_add_f16 v24, v150, v162
	v_pk_add_f16 v25, v151, v163
	s_nop 0
	v_pk_mul_f16 v22, v164, v152 clamp
	v_pk_mul_f16 v23, v165, v153 clamp
	v_pk_max_f16 v22, v24, v22
	v_pk_max_f16 v23, v25, v23
	ds_write_b64 v189, v[22:23] offset:1056
	s_waitcnt lgkmcnt(3)
	v_mfma_f32_32x32x16_f16 v[34:49], v[130:133], v[248:251], v[34:49]
	s_waitcnt vmcnt(1)
	v_pk_add_f16 v20, v142, v162
	v_pk_add_f16 v21, v143, v163
	s_nop 0
	v_pk_mul_f16 v18, v164, v144 clamp
	v_pk_mul_f16 v19, v165, v145 clamp
	v_pk_max_f16 v18, v20, v18
	v_pk_max_f16 v19, v21, v19
	ds_write_b64 v189, v[18:19] offset:1584
	ds_write2_b32 v201, v62, v63 offset1:1
	s_and_saveexec_b64 s[30:31], s[0:1]
	ds_write2_b32 v201, v64, v65 offset0:2 offset1:3
	s_or_b64 exec, exec, s[30:31]
	v_lshl_add_u64 v[158:159], s[20:21], 4, v[158:159]
	global_load_dwordx4 v[166:169], v[158:159], off
	ds_read_b128 v[50:53], v179 offset:50688
	ds_read_b128 v[54:57], v179 offset:50720
	ds_read_b128 v[58:61], v179 offset:50752
	ds_read_b128 v[62:65], v179 offset:50784
	ds_read_b128 v[160:163], v179 offset:50816
	ds_read_b128 v[240:243], v179 offset:50848
	s_waitcnt lgkmcnt(5)
	v_mfma_f32_32x32x16_f16 v[18:33], v[122:125], v[50:53], v[2:17]
	ds_read_b128 v[244:247], v179 offset:50880
	v_cvt_pk_f16_f32 v164, v34, v35
	v_cvt_pk_f16_f32 v165, v36, v37
	s_waitcnt lgkmcnt(5)
	v_mfma_f32_32x32x16_f16 v[18:33], v[98:101], v[54:57], v[18:33]
	ds_read_b128 v[34:37], v179 offset:50912
	v_exp_f16_e64 v50, v164 clamp
	v_exp_f16_e64 v51, v165 clamp
	v_exp_f16_sdwa v50, v164 clamp dst_sel:WORD_1 dst_unused:UNUSED_PRESERVE src0_sel:WORD_1
	v_exp_f16_sdwa v51, v165 clamp dst_sel:WORD_1 dst_unused:UNUSED_PRESERVE src0_sel:WORD_1
	s_nop 0
	s_waitcnt lgkmcnt(5)
	v_mfma_f32_32x32x16_f16 v[18:33], v[114:117], v[58:61], v[18:33]
	ds_read_b128 v[248:251], v179 offset:50944
	v_pk_fma_f16 v51, v51, s55, v233 op_sel_hi:[1,0,0]
	v_pk_fma_f16 v50, v50, s55, v233 op_sel_hi:[1,0,0]
	v_pk_max_f16 v51, v165, v51
	v_pk_max_f16 v50, v164, v50
	s_waitcnt lgkmcnt(5)
	v_mfma_f32_32x32x16_f16 v[18:33], v[86:89], v[62:65], v[18:33]
	ds_read_b128 v[252:255], v179 offset:50976
	v_cvt_pk_f16_f32 v52, v38, v39
	v_cvt_pk_f16_f32 v53, v40, v41
	s_waitcnt lgkmcnt(5)
	v_mfma_f32_32x32x16_f16 v[18:33], v[126:129], v[160:163], v[18:33]
	ds_read_b128 v[38:41], v179 offset:51008
	v_exp_f16_e64 v54, v52 clamp
	v_exp_f16_e64 v55, v53 clamp
	v_exp_f16_sdwa v54, v52 clamp dst_sel:WORD_1 dst_unused:UNUSED_PRESERVE src0_sel:WORD_1
	v_exp_f16_sdwa v55, v53 clamp dst_sel:WORD_1 dst_unused:UNUSED_PRESERVE src0_sel:WORD_1
	s_nop 0
	s_waitcnt lgkmcnt(5)
	v_mfma_f32_32x32x16_f16 v[18:33], v[90:93], v[240:243], v[18:33]
	ds_read_b128 v[160:163], v179 offset:51040
	v_pk_fma_f16 v55, v55, s55, v233 op_sel_hi:[1,0,0]
	v_pk_fma_f16 v54, v54, s55, v233 op_sel_hi:[1,0,0]
	v_pk_max_f16 v53, v53, v55
	v_pk_max_f16 v52, v52, v54
	s_waitcnt lgkmcnt(5)
	v_mfma_f32_32x32x16_f16 v[18:33], v[118:121], v[244:247], v[18:33]
	ds_read_b128 v[240:243], v179 offset:51072
	v_cvt_pk_f16_f32 v164, v42, v43
	v_cvt_pk_f16_f32 v165, v44, v45
	v_mfma_f32_16x16x32_f16 v[62:65], v[70:73], v[50:53], 0
	s_waitcnt lgkmcnt(5)
	v_mfma_f32_32x32x16_f16 v[18:33], v[78:81], v[34:37], v[18:33]
	ds_read_b128 v[42:45], v179 offset:51104
	v_exp_f16_e64 v244, v164 clamp
	v_exp_f16_e64 v245, v165 clamp
	v_exp_f16_sdwa v244, v164 clamp dst_sel:WORD_1 dst_unused:UNUSED_PRESERVE src0_sel:WORD_1
	v_exp_f16_sdwa v245, v165 clamp dst_sel:WORD_1 dst_unused:UNUSED_PRESERVE src0_sel:WORD_1
	s_nop 0
	s_waitcnt lgkmcnt(5)
	v_mfma_f32_32x32x16_f16 v[18:33], v[102:105], v[248:251], v[18:33]
	ds_read_b128 v[34:37], v179 offset:51136
	v_pk_fma_f16 v245, v245, s55, v233 op_sel_hi:[1,0,0]
	s_nop 0
	v_pk_max_f16 v245, v165, v245
	v_pk_fma_f16 v165, v244, s55, v233 op_sel_hi:[1,0,0]
	s_nop 0
	v_pk_max_f16 v244, v164, v165
	s_waitcnt lgkmcnt(5)
	v_mfma_f32_32x32x16_f16 v[18:33], v[74:77], v[252:255], v[18:33]
	ds_read_b128 v[248:251], v179 offset:51168
	v_cvt_pk_f16_f32 v46, v46, v47
	v_cvt_pk_f16_f32 v47, v48, v49
	s_waitcnt lgkmcnt(5)
	v_mfma_f32_32x32x16_f16 v[18:33], v[106:109], v[38:41], v[18:33]
	v_exp_f16_e64 v48, v46 clamp
	v_exp_f16_e64 v49, v47 clamp
	v_exp_f16_sdwa v48, v46 clamp dst_sel:WORD_1 dst_unused:UNUSED_PRESERVE src0_sel:WORD_1
	v_exp_f16_sdwa v49, v47 clamp dst_sel:WORD_1 dst_unused:UNUSED_PRESERVE src0_sel:WORD_1
	s_nop 0
	s_waitcnt lgkmcnt(4)
	v_mfma_f32_32x32x16_f16 v[18:33], v[82:85], v[160:163], v[18:33]
	v_pk_fma_f16 v38, v49, s55, v233 op_sel_hi:[1,0,0]
	s_nop 0
	v_pk_max_f16 v247, v47, v38
	v_pk_fma_f16 v38, v48, s55, v233 op_sel_hi:[1,0,0]
	s_nop 0
	v_pk_max_f16 v246, v46, v38
	s_waitcnt lgkmcnt(3)
	v_mfma_f32_32x32x16_f16 v[18:33], v[110:113], v[240:243], v[18:33]
	v_pk_add_f16 v40, v146, v154
	v_pk_add_f16 v41, v147, v155
	s_nop 0
	v_pk_mul_f16 v38, v156, v148 clamp
	v_pk_mul_f16 v39, v157, v149 clamp
	v_pk_max_f16 v38, v40, v38
	v_pk_max_f16 v39, v41, v39
	ds_write_b64 v189, v[38:39] offset:16896
	v_mfma_f32_16x16x32_f16 v[62:65], v[66:69], v[244:247], v[62:65]
	s_waitcnt lgkmcnt(3)
	v_mfma_f32_32x32x16_f16 v[18:33], v[94:97], v[42:45], v[18:33]
	v_pk_add_f16 v40, v138, v154
	v_pk_add_f16 v41, v139, v155
	s_nop 0
	v_pk_mul_f16 v38, v156, v140 clamp
	v_pk_mul_f16 v39, v157, v141 clamp
	v_pk_max_f16 v38, v40, v38
	v_pk_max_f16 v39, v41, v39
	ds_write_b64 v189, v[38:39] offset:17424
	s_waitcnt lgkmcnt(3)
	v_mfma_f32_32x32x16_f16 v[18:33], v[134:137], v[34:37], v[18:33]
	v_pk_add_f16 v40, v150, v154
	v_pk_add_f16 v41, v151, v155
	s_nop 0
	v_pk_mul_f16 v38, v156, v152 clamp
	v_pk_mul_f16 v39, v157, v153 clamp
	v_pk_max_f16 v38, v40, v38
	v_pk_max_f16 v39, v41, v39
	ds_write_b64 v189, v[38:39] offset:17952
	s_waitcnt lgkmcnt(3)
	v_mfma_f32_32x32x16_f16 v[18:33], v[130:133], v[248:251], v[18:33]
	v_pk_add_f16 v36, v142, v154
	v_pk_add_f16 v37, v143, v155
	s_nop 0
	v_pk_mul_f16 v34, v156, v144 clamp
	v_pk_mul_f16 v35, v157, v145 clamp
	v_pk_max_f16 v34, v36, v34
	v_pk_max_f16 v35, v37, v35
	ds_write_b64 v189, v[34:35] offset:18480
	ds_write2_b32 v211, v62, v63 offset1:1
	s_and_saveexec_b64 s[30:31], s[0:1]
	ds_write2_b32 v211, v64, v65 offset0:2 offset1:3
	s_or_b64 exec, exec, s[30:31]
	s_sub_i32 s30, 0x7d, s34
	s_mul_i32 s30, s30, 6
	s_ashr_i32 s31, s30, 31
	s_add_u32 s28, s28, s30
	s_addc_u32 s29, s29, s31
	s_and_b64 vcc, exec, s[8:9]
	s_waitcnt lgkmcnt(0)
	s_barrier
	ds_read_b128 v[50:53], v179
	ds_read_b128 v[54:57], v179 offset:32
	s_cbranch_vccnz .LBB1_110
	s_cmp_eq_u32 s41, 0
	s_cbranch_scc1 .LBB1_106
	s_and_saveexec_b64 s[30:31], s[6:7]
	s_cbranch_execz .LBB1_105
	ds_read2_b32 v[34:35], v200 offset1:224
	ds_read2_b32 v[36:37], v234 offset1:224
	ds_read2_b32 v[38:39], v235 offset1:224
	ds_read2_b32 v[40:41], v236 offset1:224
	s_lshl_b32 s35, s56, 28
	s_add_i32 s35, s35, 0xd0000000
	s_ashr_i32 s35, s35, 31
	s_waitcnt lgkmcnt(3)
	v_add_f32_e32 v34, 0, v34
	v_add_f32_e32 v34, v34, v35
	s_waitcnt lgkmcnt(2)
	v_add_f32_e32 v34, v34, v36
	v_add_f32_e32 v34, v34, v37
	s_waitcnt lgkmcnt(1)
	v_add_f32_e32 v34, v34, v38
	v_add_f32_e32 v34, v34, v39
	s_waitcnt lgkmcnt(0)
	v_add_f32_e32 v34, v34, v40
	s_and_b32 s35, s35, 0x1800
	v_add_f32_e32 v34, v34, v41
	v_add_u32_e32 v35, s35, v232
	ds_write_b32 v35, v34 offset:640

.LBB1_119:
	v_lshl_add_u64 v[154:155], s[20:21], 4, v[158:159]
	global_load_dwordx4 v[158:161], v[154:155], off
	ds_read_b128 v[58:61], v179 offset:64
	ds_read_b128 v[62:65], v179 offset:96
	ds_read_b128 v[162:165], v179 offset:128
	ds_read_b128 v[240:243], v179 offset:160
	s_waitcnt lgkmcnt(5)
	v_mfma_f32_32x32x16_f16 v[34:49], v[122:125], v[50:53], v[2:17]
	ds_read_b128 v[244:247], v179 offset:192
	v_cvt_pk_f16_f32 v156, v18, v19
	v_cvt_pk_f16_f32 v157, v20, v21
	s_waitcnt lgkmcnt(5)
	v_mfma_f32_32x32x16_f16 v[34:49], v[98:101], v[54:57], v[34:49]
	ds_read_b128 v[18:21], v179 offset:224
	v_exp_f16_e64 v50, v156 clamp
	v_exp_f16_e64 v51, v157 clamp
	v_exp_f16_sdwa v50, v156 clamp dst_sel:WORD_1 dst_unused:UNUSED_PRESERVE src0_sel:WORD_1
	v_exp_f16_sdwa v51, v157 clamp dst_sel:WORD_1 dst_unused:UNUSED_PRESERVE src0_sel:WORD_1
	s_nop 0
	s_waitcnt lgkmcnt(5)
	v_mfma_f32_32x32x16_f16 v[34:49], v[114:117], v[58:61], v[34:49]
	ds_read_b128 v[248:251], v179 offset:256
	v_pk_fma_f16 v51, v51, s55, v233 op_sel_hi:[1,0,0]
	v_pk_fma_f16 v50, v50, s55, v233 op_sel_hi:[1,0,0]
	v_pk_max_f16 v51, v157, v51
	v_pk_max_f16 v50, v156, v50
	s_waitcnt lgkmcnt(5)
	v_mfma_f32_32x32x16_f16 v[34:49], v[86:89], v[62:65], v[34:49]
	ds_read_b128 v[252:255], v179 offset:288
	v_cvt_pk_f16_f32 v52, v22, v23
	v_cvt_pk_f16_f32 v53, v24, v25
	s_waitcnt lgkmcnt(5)
	v_mfma_f32_32x32x16_f16 v[34:49], v[126:129], v[162:165], v[34:49]
	ds_read_b128 v[22:25], v179 offset:320
	v_exp_f16_e64 v54, v52 clamp
	v_exp_f16_e64 v55, v53 clamp
	v_exp_f16_sdwa v54, v52 clamp dst_sel:WORD_1 dst_unused:UNUSED_PRESERVE src0_sel:WORD_1
	v_exp_f16_sdwa v55, v53 clamp dst_sel:WORD_1 dst_unused:UNUSED_PRESERVE src0_sel:WORD_1
	s_nop 0
	s_waitcnt lgkmcnt(5)
	v_mfma_f32_32x32x16_f16 v[34:49], v[90:93], v[240:243], v[34:49]
	ds_read_b128 v[162:165], v179 offset:352
	v_pk_fma_f16 v55, v55, s55, v233 op_sel_hi:[1,0,0]
	v_pk_fma_f16 v54, v54, s55, v233 op_sel_hi:[1,0,0]
	v_pk_max_f16 v53, v53, v55
	v_pk_max_f16 v52, v52, v54
	s_waitcnt lgkmcnt(5)
	v_mfma_f32_32x32x16_f16 v[34:49], v[118:121], v[244:247], v[34:49]
	ds_read_b128 v[240:243], v179 offset:384
	v_cvt_pk_f16_f32 v156, v26, v27
	v_cvt_pk_f16_f32 v157, v28, v29
	v_mfma_f32_16x16x32_f16 v[62:65], v[70:73], v[50:53], 0
	s_waitcnt lgkmcnt(5)
	v_mfma_f32_32x32x16_f16 v[34:49], v[78:81], v[18:21], v[34:49]
	ds_read_b128 v[26:29], v179 offset:416
	v_exp_f16_e64 v244, v156 clamp
	v_exp_f16_e64 v245, v157 clamp
	v_exp_f16_sdwa v244, v156 clamp dst_sel:WORD_1 dst_unused:UNUSED_PRESERVE src0_sel:WORD_1
	v_exp_f16_sdwa v245, v157 clamp dst_sel:WORD_1 dst_unused:UNUSED_PRESERVE src0_sel:WORD_1
	s_nop 0
	s_waitcnt lgkmcnt(5)
	v_mfma_f32_32x32x16_f16 v[34:49], v[102:105], v[248:251], v[34:49]
	ds_read_b128 v[18:21], v179 offset:448
	v_pk_fma_f16 v245, v245, s55, v233 op_sel_hi:[1,0,0]
	s_nop 0
	v_pk_max_f16 v245, v157, v245
	v_pk_fma_f16 v157, v244, s55, v233 op_sel_hi:[1,0,0]
	s_nop 0
	v_pk_max_f16 v244, v156, v157
	s_waitcnt lgkmcnt(5)
	v_mfma_f32_32x32x16_f16 v[34:49], v[74:77], v[252:255], v[34:49]
	ds_read_b128 v[248:251], v179 offset:480
	v_cvt_pk_f16_f32 v30, v30, v31
	v_cvt_pk_f16_f32 v31, v32, v33
	s_waitcnt lgkmcnt(5)
	v_mfma_f32_32x32x16_f16 v[34:49], v[106:109], v[22:25], v[34:49]
	v_exp_f16_e64 v32, v30 clamp
	v_exp_f16_e64 v33, v31 clamp
	v_exp_f16_sdwa v32, v30 clamp dst_sel:WORD_1 dst_unused:UNUSED_PRESERVE src0_sel:WORD_1
	v_exp_f16_sdwa v33, v31 clamp dst_sel:WORD_1 dst_unused:UNUSED_PRESERVE src0_sel:WORD_1
	s_nop 0
	s_waitcnt lgkmcnt(4)
	v_mfma_f32_32x32x16_f16 v[34:49], v[82:85], v[162:165], v[34:49]
	v_pk_fma_f16 v22, v33, s55, v233 op_sel_hi:[1,0,0]
	s_nop 0
	v_pk_max_f16 v247, v31, v22
	v_pk_fma_f16 v22, v32, s55, v233 op_sel_hi:[1,0,0]
	s_nop 0
	v_pk_max_f16 v246, v30, v22
	s_waitcnt lgkmcnt(3)
	v_mfma_f32_32x32x16_f16 v[34:49], v[110:113], v[240:243], v[34:49]
	s_waitcnt vmcnt(2)
	v_pk_add_f16 v24, v170, v146
	v_pk_add_f16 v25, v171, v147
	s_nop 0
	v_pk_mul_f16 v22, v172, v148 clamp
	v_pk_mul_f16 v23, v173, v149 clamp
	v_pk_max_f16 v22, v24, v22
	v_pk_max_f16 v23, v25, v23
	ds_write_b64 v189, v[22:23] offset:33792
	v_mfma_f32_16x16x32_f16 v[62:65], v[66:69], v[244:247], v[62:65]
	s_waitcnt lgkmcnt(3)
	v_mfma_f32_32x32x16_f16 v[34:49], v[94:97], v[26:29], v[34:49]
	v_pk_add_f16 v24, v170, v138
	v_pk_add_f16 v25, v171, v139
	s_nop 0
	v_pk_mul_f16 v22, v172, v140 clamp
	v_pk_mul_f16 v23, v173, v141 clamp
	v_pk_max_f16 v22, v24, v22
	v_pk_max_f16 v23, v25, v23
	ds_write_b64 v189, v[22:23] offset:34320
	s_waitcnt lgkmcnt(3)
	v_mfma_f32_32x32x16_f16 v[34:49], v[134:137], v[18:21], v[34:49]
	v_pk_add_f16 v24, v170, v150
	v_pk_add_f16 v25, v171, v151
	s_nop 0
	v_pk_mul_f16 v22, v172, v152 clamp
	v_pk_mul_f16 v23, v173, v153 clamp
	v_pk_max_f16 v22, v24, v22
	v_pk_max_f16 v23, v25, v23
	ds_write_b64 v189, v[22:23] offset:34848
	s_waitcnt lgkmcnt(3)
	v_mfma_f32_32x32x16_f16 v[34:49], v[130:133], v[248:251], v[34:49]
	v_pk_add_f16 v20, v170, v142
	v_pk_add_f16 v21, v171, v143
	s_nop 0
	v_pk_mul_f16 v18, v172, v144 clamp
	v_pk_mul_f16 v19, v173, v145 clamp
	v_pk_max_f16 v18, v20, v18
	v_pk_max_f16 v19, v21, v19
	ds_write_b64 v189, v[18:19] offset:35376
	ds_write2_b32 v229, v62, v63 offset1:1
	s_and_saveexec_b64 s[30:31], s[0:1]
	ds_write2_b32 v229, v64, v65 offset0:2 offset1:3
	s_or_b64 exec, exec, s[30:31]
	s_cmp_eq_u32 s56, 16
	s_cbranch_scc0 .Lw2_sw_skip
	s_and_b64 vcc, exec, s[16:17]
	s_cbranch_vccz .Lw2_sw_skip
	v_mov_b32_dpp v70, v70 row_shl:8 row_mask:0xa bank_mask:0x3
	v_mov_b32_dpp v71, v71 row_shl:8 row_mask:0xa bank_mask:0x3
	v_mov_b32_dpp v72, v72 row_shl:8 row_mask:0xa bank_mask:0x3
	v_mov_b32_dpp v73, v73 row_shl:8 row_mask:0xa bank_mask:0x3
	v_mov_b32_dpp v66, v66 row_shl:8 row_mask:0xa bank_mask:0x3
	v_mov_b32_dpp v67, v67 row_shl:8 row_mask:0xa bank_mask:0x3
	v_mov_b32_dpp v68, v68 row_shl:8 row_mask:0xa bank_mask:0x3
	v_mov_b32_dpp v69, v69 row_shl:8 row_mask:0xa bank_mask:0x3
.Lw2_sw_skip:
	v_lshl_add_u64 v[154:155], s[20:21], 4, v[154:155]
	global_load_dwordx4 v[162:165], v[154:155], off
	ds_read_b128 v[50:53], v179 offset:16896
	ds_read_b128 v[54:57], v179 offset:16928
	ds_read_b128 v[58:61], v179 offset:16960
	ds_read_b128 v[62:65], v179 offset:16992
	ds_read_b128 v[170:173], v179 offset:17024
	ds_read_b128 v[240:243], v179 offset:17056
	s_waitcnt lgkmcnt(5)
	v_mfma_f32_32x32x16_f16 v[18:33], v[122:125], v[50:53], v[2:17]
	ds_read_b128 v[244:247], v179 offset:17088
	v_cvt_pk_f16_f32 v156, v34, v35
	v_cvt_pk_f16_f32 v157, v36, v37
	s_waitcnt lgkmcnt(5)
	v_mfma_f32_32x32x16_f16 v[18:33], v[98:101], v[54:57], v[18:33]
	ds_read_b128 v[34:37], v179 offset:17120
	v_exp_f16_e64 v50, v156 clamp
	v_exp_f16_e64 v51, v157 clamp
	v_exp_f16_sdwa v50, v156 clamp dst_sel:WORD_1 dst_unused:UNUSED_PRESERVE src0_sel:WORD_1
	v_exp_f16_sdwa v51, v157 clamp dst_sel:WORD_1 dst_unused:UNUSED_PRESERVE src0_sel:WORD_1
	s_nop 0
	s_waitcnt lgkmcnt(5)
	v_mfma_f32_32x32x16_f16 v[18:33], v[114:117], v[58:61], v[18:33]
	ds_read_b128 v[248:251], v179 offset:17152
	v_pk_fma_f16 v51, v51, s55, v233 op_sel_hi:[1,0,0]
	v_pk_fma_f16 v50, v50, s55, v233 op_sel_hi:[1,0,0]
	v_pk_max_f16 v51, v157, v51
	v_pk_max_f16 v50, v156, v50
	s_waitcnt lgkmcnt(5)
	v_mfma_f32_32x32x16_f16 v[18:33], v[86:89], v[62:65], v[18:33]
	ds_read_b128 v[252:255], v179 offset:17184
	v_cvt_pk_f16_f32 v52, v38, v39
	v_cvt_pk_f16_f32 v53, v40, v41
	s_waitcnt lgkmcnt(5)
	v_mfma_f32_32x32x16_f16 v[18:33], v[126:129], v[170:173], v[18:33]
	ds_read_b128 v[38:41], v179 offset:17216
	v_exp_f16_e64 v54, v52 clamp
	v_exp_f16_e64 v55, v53 clamp
	v_exp_f16_sdwa v54, v52 clamp dst_sel:WORD_1 dst_unused:UNUSED_PRESERVE src0_sel:WORD_1
	v_exp_f16_sdwa v55, v53 clamp dst_sel:WORD_1 dst_unused:UNUSED_PRESERVE src0_sel:WORD_1
	s_nop 0
	s_waitcnt lgkmcnt(5)
	v_mfma_f32_32x32x16_f16 v[18:33], v[90:93], v[240:243], v[18:33]
	ds_read_b128 v[170:173], v179 offset:17248
	v_pk_fma_f16 v55, v55, s55, v233 op_sel_hi:[1,0,0]
	v_pk_fma_f16 v54, v54, s55, v233 op_sel_hi:[1,0,0]
	v_pk_max_f16 v53, v53, v55
	v_pk_max_f16 v52, v52, v54
	s_waitcnt lgkmcnt(5)
	v_mfma_f32_32x32x16_f16 v[18:33], v[118:121], v[244:247], v[18:33]
	ds_read_b128 v[240:243], v179 offset:17280
	v_cvt_pk_f16_f32 v156, v42, v43
	v_cvt_pk_f16_f32 v157, v44, v45
	v_mfma_f32_16x16x32_f16 v[62:65], v[70:73], v[50:53], 0
	s_waitcnt lgkmcnt(5)
	v_mfma_f32_32x32x16_f16 v[18:33], v[78:81], v[34:37], v[18:33]
	ds_read_b128 v[42:45], v179 offset:17312
	v_exp_f16_e64 v244, v156 clamp
	v_exp_f16_e64 v245, v157 clamp
	v_exp_f16_sdwa v244, v156 clamp dst_sel:WORD_1 dst_unused:UNUSED_PRESERVE src0_sel:WORD_1
	v_exp_f16_sdwa v245, v157 clamp dst_sel:WORD_1 dst_unused:UNUSED_PRESERVE src0_sel:WORD_1
	s_nop 0
	s_waitcnt lgkmcnt(5)
	v_mfma_f32_32x32x16_f16 v[18:33], v[102:105], v[248:251], v[18:33]
	ds_read_b128 v[34:37], v179 offset:17344
	v_pk_fma_f16 v245, v245, s55, v233 op_sel_hi:[1,0,0]
	s_nop 0
	v_pk_max_f16 v245, v157, v245
	v_pk_fma_f16 v157, v244, s55, v233 op_sel_hi:[1,0,0]
	s_nop 0
	v_pk_max_f16 v244, v156, v157
	s_waitcnt lgkmcnt(5)
	v_mfma_f32_32x32x16_f16 v[18:33], v[74:77], v[252:255], v[18:33]
	ds_read_b128 v[248:251], v179 offset:17376
	v_cvt_pk_f16_f32 v46, v46, v47
	v_cvt_pk_f16_f32 v47, v48, v49
	s_waitcnt lgkmcnt(5)
	v_mfma_f32_32x32x16_f16 v[18:33], v[106:109], v[38:41], v[18:33]
	v_exp_f16_e64 v48, v46 clamp
	v_exp_f16_e64 v49, v47 clamp
	v_exp_f16_sdwa v48, v46 clamp dst_sel:WORD_1 dst_unused:UNUSED_PRESERVE src0_sel:WORD_1
	v_exp_f16_sdwa v49, v47 clamp dst_sel:WORD_1 dst_unused:UNUSED_PRESERVE src0_sel:WORD_1
	s_nop 0
	s_waitcnt lgkmcnt(4)
	v_mfma_f32_32x32x16_f16 v[18:33], v[82:85], v[170:173], v[18:33]
	v_pk_fma_f16 v38, v49, s55, v233 op_sel_hi:[1,0,0]
	s_nop 0
	v_pk_max_f16 v247, v47, v38
	v_pk_fma_f16 v38, v48, s55, v233 op_sel_hi:[1,0,0]
	s_nop 0
	v_pk_max_f16 v246, v46, v38
	s_waitcnt lgkmcnt(3)
	v_mfma_f32_32x32x16_f16 v[18:33], v[110:113], v[240:243], v[18:33]
	s_waitcnt vmcnt(2)
	v_pk_add_f16 v40, v166, v146
	v_pk_add_f16 v41, v167, v147
	s_nop 0
	v_pk_mul_f16 v38, v168, v148 clamp
	v_pk_mul_f16 v39, v169, v149 clamp
	v_pk_max_f16 v38, v40, v38
	v_pk_max_f16 v39, v41, v39
	ds_write_b64 v189, v[38:39] offset:50688
	v_mfma_f32_16x16x32_f16 v[62:65], v[66:69], v[244:247], v[62:65]
	s_waitcnt lgkmcnt(3)
	v_mfma_f32_32x32x16_f16 v[18:33], v[94:97], v[42:45], v[18:33]
	v_pk_add_f16 v40, v166, v138
	v_pk_add_f16 v41, v167, v139
	s_nop 0
	v_pk_mul_f16 v38, v168, v140 clamp
	v_pk_mul_f16 v39, v169, v141 clamp
	v_pk_max_f16 v38, v40, v38
	v_pk_max_f16 v39, v41, v39
	ds_write_b64 v189, v[38:39] offset:51216
	s_waitcnt lgkmcnt(3)
	v_mfma_f32_32x32x16_f16 v[18:33], v[134:137], v[34:37], v[18:33]
	v_pk_add_f16 v40, v166, v150
	v_pk_add_f16 v41, v167, v151
	s_nop 0
	v_pk_mul_f16 v38, v168, v152 clamp
	v_pk_mul_f16 v39, v169, v153 clamp
	v_pk_max_f16 v38, v40, v38
	v_pk_max_f16 v39, v41, v39
	ds_write_b64 v189, v[38:39] offset:51744
	s_waitcnt lgkmcnt(3)
	v_mfma_f32_32x32x16_f16 v[18:33], v[130:133], v[248:251], v[18:33]
	v_pk_add_f16 v36, v166, v142
	v_pk_add_f16 v37, v167, v143
	s_nop 0
	v_pk_mul_f16 v34, v168, v144 clamp
	v_pk_mul_f16 v35, v169, v145 clamp
	v_pk_max_f16 v34, v36, v34
	v_pk_max_f16 v35, v37, v35
	ds_write_b64 v189, v[34:35] offset:52272
	ds_write2_b32 v206, v62, v63 offset1:1
	s_and_saveexec_b64 s[30:31], s[0:1]
	ds_write2_b32 v206, v64, v65 offset0:2 offset1:3
	s_or_b64 exec, exec, s[30:31]
	s_add_i32 s34, s34, 1
	s_sub_i32 s30, 0x7d, s34
	s_mul_i32 s30, s30, 6
	s_ashr_i32 s31, s30, 31
	s_add_u32 s28, s28, s30
	s_addc_u32 s29, s29, s31
	s_and_b64 vcc, exec, s[8:9]
	s_waitcnt lgkmcnt(0)
	s_barrier
	ds_read_b128 v[50:53], v179 offset:33792
	ds_read_b128 v[54:57], v179 offset:33824
	s_cbranch_vccnz .LBB1_136
	s_cmp_eq_u32 s41, 0
	s_cbranch_scc1 .LBB1_132
	s_and_saveexec_b64 s[30:31], s[6:7]
	s_cbranch_execz .LBB1_131
	ds_read2_b32 v[34:35], v180 offset1:224
	v_add_u32_e32 v36, 0x700, v180
	ds_read2_b32 v[36:37], v36 offset1:224
	v_add_u32_e32 v38, 0xe00, v180
	s_lshl_b32 s35, s56, 28
	s_waitcnt lgkmcnt(1)
	v_add_f32_e32 v34, 0, v34
	v_add_f32_e32 v40, v34, v35
	ds_read2_b32 v[34:35], v38 offset1:224
	v_add_u32_e32 v38, 0x1500, v180
	ds_read2_b32 v[38:39], v38 offset1:224
	s_waitcnt lgkmcnt(2)
	v_add_f32_e32 v36, v40, v36
	v_add_f32_e32 v36, v36, v37
	s_waitcnt lgkmcnt(1)
	v_add_f32_e32 v34, v36, v34
	s_add_i32 s35, s35, 0xf0000000
	v_add_f32_e32 v34, v34, v35
	s_ashr_i32 s35, s35, 31
	s_waitcnt lgkmcnt(0)
	v_add_f32_e32 v34, v34, v38
	s_and_b32 s35, s35, 0x1800
	v_add_f32_e32 v34, v34, v39
	v_add_u32_e32 v35, s35, v232
	ds_write_b32 v35, v34 offset:896

.LBB1_145:
	v_lshl_add_u64 v[166:167], s[20:21], 4, v[154:155]
	global_load_dwordx4 v[154:157], v[166:167], off
	ds_read_b128 v[58:61], v179 offset:33856
	ds_read_b128 v[62:65], v179 offset:33888
	ds_read_b128 v[168:171], v179 offset:33920
	ds_read_b128 v[240:243], v179 offset:33952
	s_waitcnt lgkmcnt(5)
	v_mfma_f32_32x32x16_f16 v[34:49], v[122:125], v[50:53], v[2:17]
	ds_read_b128 v[244:247], v179 offset:33984
	v_cvt_pk_f16_f32 v172, v18, v19
	v_cvt_pk_f16_f32 v173, v20, v21
	s_waitcnt lgkmcnt(5)
	v_mfma_f32_32x32x16_f16 v[34:49], v[98:101], v[54:57], v[34:49]
	ds_read_b128 v[18:21], v179 offset:34016
	v_exp_f16_e64 v50, v172 clamp
	v_exp_f16_e64 v51, v173 clamp
	v_exp_f16_sdwa v50, v172 clamp dst_sel:WORD_1 dst_unused:UNUSED_PRESERVE src0_sel:WORD_1
	v_exp_f16_sdwa v51, v173 clamp dst_sel:WORD_1 dst_unused:UNUSED_PRESERVE src0_sel:WORD_1
	s_nop 0
	s_waitcnt lgkmcnt(5)
	v_mfma_f32_32x32x16_f16 v[34:49], v[114:117], v[58:61], v[34:49]
	ds_read_b128 v[248:251], v179 offset:34048
	v_pk_fma_f16 v51, v51, s55, v233 op_sel_hi:[1,0,0]
	v_pk_fma_f16 v50, v50, s55, v233 op_sel_hi:[1,0,0]
	v_pk_max_f16 v51, v173, v51
	v_pk_max_f16 v50, v172, v50
	s_waitcnt lgkmcnt(5)
	v_mfma_f32_32x32x16_f16 v[34:49], v[86:89], v[62:65], v[34:49]
	ds_read_b128 v[252:255], v179 offset:34080
	v_cvt_pk_f16_f32 v52, v22, v23
	v_cvt_pk_f16_f32 v53, v24, v25
	s_waitcnt lgkmcnt(5)
	v_mfma_f32_32x32x16_f16 v[34:49], v[126:129], v[168:171], v[34:49]
	ds_read_b128 v[22:25], v179 offset:34112
	v_exp_f16_e64 v54, v52 clamp
	v_exp_f16_e64 v55, v53 clamp
	v_exp_f16_sdwa v54, v52 clamp dst_sel:WORD_1 dst_unused:UNUSED_PRESERVE src0_sel:WORD_1
	v_exp_f16_sdwa v55, v53 clamp dst_sel:WORD_1 dst_unused:UNUSED_PRESERVE src0_sel:WORD_1
	s_nop 0
	s_waitcnt lgkmcnt(5)
	v_mfma_f32_32x32x16_f16 v[34:49], v[90:93], v[240:243], v[34:49]
	ds_read_b128 v[168:171], v179 offset:34144
	v_pk_fma_f16 v55, v55, s55, v233 op_sel_hi:[1,0,0]
	v_pk_fma_f16 v54, v54, s55, v233 op_sel_hi:[1,0,0]
	v_pk_max_f16 v53, v53, v55
	v_pk_max_f16 v52, v52, v54
	s_waitcnt lgkmcnt(5)
	v_mfma_f32_32x32x16_f16 v[34:49], v[118:121], v[244:247], v[34:49]
	ds_read_b128 v[240:243], v179 offset:34176
	v_cvt_pk_f16_f32 v172, v26, v27
	v_cvt_pk_f16_f32 v173, v28, v29
	v_mfma_f32_16x16x32_f16 v[62:65], v[70:73], v[50:53], 0
	s_waitcnt lgkmcnt(5)
	v_mfma_f32_32x32x16_f16 v[34:49], v[78:81], v[18:21], v[34:49]
	ds_read_b128 v[26:29], v179 offset:34208
	v_exp_f16_e64 v244, v172 clamp
	v_exp_f16_e64 v245, v173 clamp
	v_exp_f16_sdwa v244, v172 clamp dst_sel:WORD_1 dst_unused:UNUSED_PRESERVE src0_sel:WORD_1
	v_exp_f16_sdwa v245, v173 clamp dst_sel:WORD_1 dst_unused:UNUSED_PRESERVE src0_sel:WORD_1
	s_nop 0
	s_waitcnt lgkmcnt(5)
	v_mfma_f32_32x32x16_f16 v[34:49], v[102:105], v[248:251], v[34:49]
	ds_read_b128 v[18:21], v179 offset:34240
	v_pk_fma_f16 v245, v245, s55, v233 op_sel_hi:[1,0,0]
	s_nop 0
	v_pk_max_f16 v245, v173, v245
	v_pk_fma_f16 v173, v244, s55, v233 op_sel_hi:[1,0,0]
	s_nop 0
	v_pk_max_f16 v244, v172, v173
	s_waitcnt lgkmcnt(5)
	v_mfma_f32_32x32x16_f16 v[34:49], v[74:77], v[252:255], v[34:49]
	ds_read_b128 v[248:251], v179 offset:34272
	v_cvt_pk_f16_f32 v30, v30, v31
	v_cvt_pk_f16_f32 v31, v32, v33
	s_waitcnt lgkmcnt(5)
	v_mfma_f32_32x32x16_f16 v[34:49], v[106:109], v[22:25], v[34:49]
	v_exp_f16_e64 v32, v30 clamp
	v_exp_f16_e64 v33, v31 clamp
	v_exp_f16_sdwa v32, v30 clamp dst_sel:WORD_1 dst_unused:UNUSED_PRESERVE src0_sel:WORD_1
	v_exp_f16_sdwa v33, v31 clamp dst_sel:WORD_1 dst_unused:UNUSED_PRESERVE src0_sel:WORD_1
	s_nop 0
	s_waitcnt lgkmcnt(4)
	v_mfma_f32_32x32x16_f16 v[34:49], v[82:85], v[168:171], v[34:49]
	v_pk_fma_f16 v22, v33, s55, v233 op_sel_hi:[1,0,0]
	s_nop 0
	v_pk_max_f16 v247, v31, v22
	v_pk_fma_f16 v22, v32, s55, v233 op_sel_hi:[1,0,0]
	s_nop 0
	v_pk_max_f16 v246, v30, v22
	s_waitcnt lgkmcnt(3)
	v_mfma_f32_32x32x16_f16 v[34:49], v[110:113], v[240:243], v[34:49]
	s_waitcnt vmcnt(2)
	v_pk_add_f16 v24, v146, v158
	v_pk_add_f16 v25, v147, v159
	s_nop 0
	v_pk_mul_f16 v22, v160, v148 clamp
	v_pk_mul_f16 v23, v161, v149 clamp
	v_pk_max_f16 v22, v24, v22
	v_pk_max_f16 v23, v25, v23
	ds_write_b64 v189, v[22:23]
	v_mfma_f32_16x16x32_f16 v[62:65], v[66:69], v[244:247], v[62:65]
	s_waitcnt lgkmcnt(3)
	v_mfma_f32_32x32x16_f16 v[34:49], v[94:97], v[26:29], v[34:49]
	v_pk_add_f16 v24, v138, v158
	v_pk_add_f16 v25, v139, v159
	s_nop 0
	v_pk_mul_f16 v22, v160, v140 clamp
	v_pk_mul_f16 v23, v161, v141 clamp
	v_pk_max_f16 v22, v24, v22
	v_pk_max_f16 v23, v25, v23
	ds_write_b64 v189, v[22:23] offset:528
	s_waitcnt lgkmcnt(3)
	v_mfma_f32_32x32x16_f16 v[34:49], v[134:137], v[18:21], v[34:49]
	v_pk_add_f16 v24, v150, v158
	v_pk_add_f16 v25, v151, v159
	s_nop 0
	v_pk_mul_f16 v22, v160, v152 clamp
	v_pk_mul_f16 v23, v161, v153 clamp
	v_pk_max_f16 v22, v24, v22
	v_pk_max_f16 v23, v25, v23
	ds_write_b64 v189, v[22:23] offset:1056
	s_waitcnt lgkmcnt(3)
	v_mfma_f32_32x32x16_f16 v[34:49], v[130:133], v[248:251], v[34:49]
	v_pk_add_f16 v20, v142, v158
	v_pk_add_f16 v21, v143, v159
	s_nop 0
	v_pk_mul_f16 v18, v160, v144 clamp
	v_pk_mul_f16 v19, v161, v145 clamp
	v_pk_max_f16 v18, v20, v18
	v_pk_max_f16 v19, v21, v19
	ds_write_b64 v189, v[18:19] offset:1584
	ds_write2_b32 v201, v62, v63 offset1:1
	s_and_saveexec_b64 s[30:31], s[0:1]
	ds_write2_b32 v201, v64, v65 offset0:2 offset1:3
	s_or_b64 exec, exec, s[30:31]
	v_lshl_add_u64 v[166:167], s[20:21], 4, v[166:167]
	global_load_dwordx4 v[158:161], v[166:167], off
	ds_read_b128 v[50:53], v179 offset:50688
	ds_read_b128 v[54:57], v179 offset:50720
	ds_read_b128 v[58:61], v179 offset:50752
	ds_read_b128 v[62:65], v179 offset:50784
	ds_read_b128 v[168:171], v179 offset:50816
	ds_read_b128 v[240:243], v179 offset:50848
	s_waitcnt lgkmcnt(5)
	v_mfma_f32_32x32x16_f16 v[18:33], v[122:125], v[50:53], v[2:17]
	ds_read_b128 v[244:247], v179 offset:50880
	v_cvt_pk_f16_f32 v172, v34, v35
	v_cvt_pk_f16_f32 v173, v36, v37
	s_waitcnt lgkmcnt(5)
	v_mfma_f32_32x32x16_f16 v[18:33], v[98:101], v[54:57], v[18:33]
	ds_read_b128 v[34:37], v179 offset:50912
	v_exp_f16_e64 v50, v172 clamp
	v_exp_f16_e64 v51, v173 clamp
	v_exp_f16_sdwa v50, v172 clamp dst_sel:WORD_1 dst_unused:UNUSED_PRESERVE src0_sel:WORD_1
	v_exp_f16_sdwa v51, v173 clamp dst_sel:WORD_1 dst_unused:UNUSED_PRESERVE src0_sel:WORD_1
	s_nop 0
	s_waitcnt lgkmcnt(5)
	v_mfma_f32_32x32x16_f16 v[18:33], v[114:117], v[58:61], v[18:33]
	ds_read_b128 v[248:251], v179 offset:50944
	v_pk_fma_f16 v51, v51, s55, v233 op_sel_hi:[1,0,0]
	v_pk_fma_f16 v50, v50, s55, v233 op_sel_hi:[1,0,0]
	v_pk_max_f16 v51, v173, v51
	v_pk_max_f16 v50, v172, v50
	s_waitcnt lgkmcnt(5)
	v_mfma_f32_32x32x16_f16 v[18:33], v[86:89], v[62:65], v[18:33]
	ds_read_b128 v[252:255], v179 offset:50976
	v_cvt_pk_f16_f32 v52, v38, v39
	v_cvt_pk_f16_f32 v53, v40, v41
	s_waitcnt lgkmcnt(5)
	v_mfma_f32_32x32x16_f16 v[18:33], v[126:129], v[168:171], v[18:33]
	ds_read_b128 v[38:41], v179 offset:51008
	v_exp_f16_e64 v54, v52 clamp
	v_exp_f16_e64 v55, v53 clamp
	v_exp_f16_sdwa v54, v52 clamp dst_sel:WORD_1 dst_unused:UNUSED_PRESERVE src0_sel:WORD_1
	v_exp_f16_sdwa v55, v53 clamp dst_sel:WORD_1 dst_unused:UNUSED_PRESERVE src0_sel:WORD_1
	s_nop 0
	s_waitcnt lgkmcnt(5)
	v_mfma_f32_32x32x16_f16 v[18:33], v[90:93], v[240:243], v[18:33]
	ds_read_b128 v[168:171], v179 offset:51040
	v_pk_fma_f16 v55, v55, s55, v233 op_sel_hi:[1,0,0]
	v_pk_fma_f16 v54, v54, s55, v233 op_sel_hi:[1,0,0]
	v_pk_max_f16 v53, v53, v55
	v_pk_max_f16 v52, v52, v54
	s_waitcnt lgkmcnt(5)
	v_mfma_f32_32x32x16_f16 v[18:33], v[118:121], v[244:247], v[18:33]
	ds_read_b128 v[240:243], v179 offset:51072
	v_cvt_pk_f16_f32 v172, v42, v43
	v_cvt_pk_f16_f32 v173, v44, v45
	v_mfma_f32_16x16x32_f16 v[62:65], v[70:73], v[50:53], 0
	s_waitcnt lgkmcnt(5)
	v_mfma_f32_32x32x16_f16 v[18:33], v[78:81], v[34:37], v[18:33]
	ds_read_b128 v[42:45], v179 offset:51104
	v_exp_f16_e64 v244, v172 clamp
	v_exp_f16_e64 v245, v173 clamp
	v_exp_f16_sdwa v244, v172 clamp dst_sel:WORD_1 dst_unused:UNUSED_PRESERVE src0_sel:WORD_1
	v_exp_f16_sdwa v245, v173 clamp dst_sel:WORD_1 dst_unused:UNUSED_PRESERVE src0_sel:WORD_1
	s_nop 0
	s_waitcnt lgkmcnt(5)
	v_mfma_f32_32x32x16_f16 v[18:33], v[102:105], v[248:251], v[18:33]
	ds_read_b128 v[34:37], v179 offset:51136
	v_pk_fma_f16 v245, v245, s55, v233 op_sel_hi:[1,0,0]
	s_nop 0
	v_pk_max_f16 v245, v173, v245
	v_pk_fma_f16 v173, v244, s55, v233 op_sel_hi:[1,0,0]
	s_nop 0
	v_pk_max_f16 v244, v172, v173
	s_waitcnt lgkmcnt(5)
	v_mfma_f32_32x32x16_f16 v[18:33], v[74:77], v[252:255], v[18:33]
	ds_read_b128 v[248:251], v179 offset:51168
	v_cvt_pk_f16_f32 v46, v46, v47
	v_cvt_pk_f16_f32 v47, v48, v49
	s_waitcnt lgkmcnt(5)
	v_mfma_f32_32x32x16_f16 v[18:33], v[106:109], v[38:41], v[18:33]
	v_exp_f16_e64 v48, v46 clamp
	v_exp_f16_e64 v49, v47 clamp
	v_exp_f16_sdwa v48, v46 clamp dst_sel:WORD_1 dst_unused:UNUSED_PRESERVE src0_sel:WORD_1
	v_exp_f16_sdwa v49, v47 clamp dst_sel:WORD_1 dst_unused:UNUSED_PRESERVE src0_sel:WORD_1
	s_nop 0
	s_waitcnt lgkmcnt(4)
	v_mfma_f32_32x32x16_f16 v[18:33], v[82:85], v[168:171], v[18:33]
	v_pk_fma_f16 v38, v49, s55, v233 op_sel_hi:[1,0,0]
	s_nop 0
	v_pk_max_f16 v247, v47, v38
	v_pk_fma_f16 v38, v48, s55, v233 op_sel_hi:[1,0,0]
	s_nop 0
	v_pk_max_f16 v246, v46, v38
	s_waitcnt lgkmcnt(3)
	v_mfma_f32_32x32x16_f16 v[18:33], v[110:113], v[240:243], v[18:33]
	s_waitcnt vmcnt(2)
	v_pk_add_f16 v40, v146, v162
	v_pk_add_f16 v41, v147, v163
	s_nop 0
	v_pk_mul_f16 v38, v164, v148 clamp
	v_pk_mul_f16 v39, v165, v149 clamp
	v_pk_max_f16 v38, v40, v38
	v_pk_max_f16 v39, v41, v39
	ds_write_b64 v189, v[38:39] offset:16896
	v_mfma_f32_16x16x32_f16 v[62:65], v[66:69], v[244:247], v[62:65]
	s_waitcnt lgkmcnt(3)
	v_mfma_f32_32x32x16_f16 v[18:33], v[94:97], v[42:45], v[18:33]
	v_pk_add_f16 v40, v138, v162
	v_pk_add_f16 v41, v139, v163
	s_nop 0
	v_pk_mul_f16 v38, v164, v140 clamp
	v_pk_mul_f16 v39, v165, v141 clamp
	v_pk_max_f16 v38, v40, v38
	v_pk_max_f16 v39, v41, v39
	ds_write_b64 v189, v[38:39] offset:17424
	s_waitcnt lgkmcnt(3)
	v_mfma_f32_32x32x16_f16 v[18:33], v[134:137], v[34:37], v[18:33]
	v_pk_add_f16 v40, v150, v162
	v_pk_add_f16 v41, v151, v163
	s_nop 0
	v_pk_mul_f16 v38, v164, v152 clamp
	v_pk_mul_f16 v39, v165, v153 clamp
	v_pk_max_f16 v38, v40, v38
	v_pk_max_f16 v39, v41, v39
	ds_write_b64 v189, v[38:39] offset:17952
	s_waitcnt lgkmcnt(3)
	v_mfma_f32_32x32x16_f16 v[18:33], v[130:133], v[248:251], v[18:33]
	v_pk_add_f16 v36, v142, v162
	v_pk_add_f16 v37, v143, v163
	s_nop 0
	v_pk_mul_f16 v34, v164, v144 clamp
	v_pk_mul_f16 v35, v165, v145 clamp
	v_pk_max_f16 v34, v36, v34
	v_pk_max_f16 v35, v37, v35
	ds_write_b64 v189, v[34:35] offset:18480
	ds_write2_b32 v211, v62, v63 offset1:1
	s_and_saveexec_b64 s[30:31], s[0:1]
	ds_write2_b32 v211, v64, v65 offset0:2 offset1:3
	s_or_b64 exec, exec, s[30:31]
	s_add_i32 s35, s34, 1
	s_add_i32 s34, s56, 8
	s_cmp_eq_u32 s56, 8
	s_cselect_b64 vcc, -1, 0
	s_and_b64 s[30:31], vcc, exec
	v_lshl_add_u64 v[34:35], s[20:21], 4, v[166:167]
	s_cselect_b32 s20, s44, s20
	s_add_i32 s35, s35, 1
	s_and_b64 s[26:27], exec, s[26:27]
	s_cselect_b32 s30, s51, s35
	s_sub_i32 s26, 0x7e, s30
	s_mul_i32 s26, s26, 6
	s_ashr_i32 s27, s26, 31
	s_add_u32 s26, s28, s26
	s_addc_u32 s27, s29, s27
	s_add_i32 s31, s30, 1
	s_add_i32 s48, s48, 2
	s_add_i32 s54, s54, 16
	v_cndmask_b32_e32 v169, v35, v175, vcc
	v_cndmask_b32_e32 v168, v34, v174, vcc
	s_cmp_eq_u32 s34, 32
	s_waitcnt lgkmcnt(0)
	s_barrier
	s_cbranch_scc1 .LBB1_155
	ds_read_b128 v[50:53], v179
	ds_read_b128 v[54:57], v179 offset:32
	s_mov_b32 s56, s34
	s_and_b64 vcc, exec, s[8:9]
	s_cbranch_vccz .LBB1_42
	s_branch .LBB1_50
.LBB1_155:
	ds_read_b128 v[50:53], v179
	ds_read_b128 v[54:57], v179 offset:32
	s_and_b64 vcc, exec, s[24:25]
	s_cbranch_vccz .LBB1_164
	s_cmp_lg_u32 s41, 0
	s_cbranch_scc0 .LBB1_160
	s_and_saveexec_b64 s[12:13], s[6:7]
	s_cbranch_execz .LBB1_159
	ds_read2_b32 v[34:35], v200 offset1:224
	v_add_u32_e32 v36, 0x700, v200
	v_add_u32_e32 v38, 0xe00, v200
	ds_read2_b32 v[36:37], v36 offset1:224
	ds_read2_b32 v[38:39], v38 offset1:224
	s_waitcnt lgkmcnt(2)
	v_add_f32_e32 v34, 0, v34
	v_add_f32_e32 v40, v34, v35
	v_add_u32_e32 v34, 0x1500, v200
	ds_read2_b32 v[34:35], v34 offset1:224
	s_waitcnt lgkmcnt(2)
	v_add_f32_e32 v36, v40, v36
	v_add_f32_e32 v36, v36, v37
	s_waitcnt lgkmcnt(1)
	v_add_f32_e32 v36, v36, v38
	v_add_f32_e32 v36, v36, v39
	s_waitcnt lgkmcnt(0)
	v_add_f32_e32 v34, v36, v34
	v_add_f32_e32 v34, v34, v35
	v_mov_b32_e32 v35, 0x19080
	v_lshl_add_u32 v35, v177, 2, v35
	ds_write_b32 v35, v34

.LBB1_173:
	ds_read_b128 v[58:61], v179 offset:64
	ds_read_b128 v[62:65], v179 offset:96
	ds_read_b128 v[162:165], v179 offset:128
	ds_read_b128 v[166:169], v179 offset:160
	s_waitcnt lgkmcnt(5)
	v_mfma_f32_32x32x16_f16 v[34:49], v[122:125], v[50:53], v[2:17]
	ds_read_b128 v[170:173], v179 offset:192
	v_cvt_pk_f16_f32 v174, v18, v19
	v_cvt_pk_f16_f32 v175, v20, v21
	s_waitcnt lgkmcnt(5)
	v_mfma_f32_32x32x16_f16 v[34:49], v[98:101], v[54:57], v[34:49]
	ds_read_b128 v[18:21], v179 offset:224
	v_exp_f16_e64 v50, v174 clamp
	v_exp_f16_e64 v51, v175 clamp
	v_exp_f16_sdwa v50, v174 clamp dst_sel:WORD_1 dst_unused:UNUSED_PRESERVE src0_sel:WORD_1
	v_exp_f16_sdwa v51, v175 clamp dst_sel:WORD_1 dst_unused:UNUSED_PRESERVE src0_sel:WORD_1
	s_nop 0
	s_waitcnt lgkmcnt(5)
	v_mfma_f32_32x32x16_f16 v[34:49], v[114:117], v[58:61], v[34:49]
	ds_read_b128 v[230:233], v179 offset:256
	s_movk_i32 s20, 0x3dc5
	v_mov_b32_e32 v199, 0xbdc5
	v_pk_fma_f16 v51, v51, s20, v199 op_sel_hi:[1,0,0]
	v_pk_fma_f16 v50, v50, s20, v199 op_sel_hi:[1,0,0]
	v_pk_max_f16 v51, v175, v51
	v_pk_max_f16 v50, v174, v50
	s_waitcnt lgkmcnt(5)
	v_mfma_f32_32x32x16_f16 v[34:49], v[86:89], v[62:65], v[34:49]
	ds_read_b128 v[234:237], v179 offset:288
	v_cvt_pk_f16_f32 v52, v22, v23
	v_cvt_pk_f16_f32 v53, v24, v25
	s_waitcnt lgkmcnt(5)
	v_mfma_f32_32x32x16_f16 v[34:49], v[126:129], v[162:165], v[34:49]
	ds_read_b128 v[22:25], v179 offset:320
	v_exp_f16_e64 v54, v52 clamp
	v_exp_f16_e64 v55, v53 clamp
	v_exp_f16_sdwa v54, v52 clamp dst_sel:WORD_1 dst_unused:UNUSED_PRESERVE src0_sel:WORD_1
	v_exp_f16_sdwa v55, v53 clamp dst_sel:WORD_1 dst_unused:UNUSED_PRESERVE src0_sel:WORD_1
	s_nop 0
	s_waitcnt lgkmcnt(5)
	v_mfma_f32_32x32x16_f16 v[34:49], v[90:93], v[166:169], v[34:49]
	ds_read_b128 v[162:165], v179 offset:352
	v_pk_fma_f16 v55, v55, s20, v199 op_sel_hi:[1,0,0]
	v_pk_fma_f16 v54, v54, s20, v199 op_sel_hi:[1,0,0]
	v_pk_max_f16 v53, v53, v55
	v_pk_max_f16 v52, v52, v54
	s_waitcnt lgkmcnt(5)
	v_mfma_f32_32x32x16_f16 v[34:49], v[118:121], v[170:173], v[34:49]
	ds_read_b128 v[166:169], v179 offset:384
	v_cvt_pk_f16_f32 v170, v26, v27
	v_cvt_pk_f16_f32 v171, v28, v29
	v_mfma_f32_16x16x32_f16 v[62:65], v[70:73], v[50:53], 0
	s_waitcnt lgkmcnt(5)
	v_mfma_f32_32x32x16_f16 v[34:49], v[78:81], v[18:21], v[34:49]
	ds_read_b128 v[26:29], v179 offset:416
	v_exp_f16_e64 v172, v170 clamp
	v_exp_f16_e64 v173, v171 clamp
	v_exp_f16_sdwa v172, v170 clamp dst_sel:WORD_1 dst_unused:UNUSED_PRESERVE src0_sel:WORD_1
	v_exp_f16_sdwa v173, v171 clamp dst_sel:WORD_1 dst_unused:UNUSED_PRESERVE src0_sel:WORD_1
	s_nop 0
	s_waitcnt lgkmcnt(5)
	v_mfma_f32_32x32x16_f16 v[34:49], v[102:105], v[230:233], v[34:49]
	ds_read_b128 v[18:21], v179 offset:448
	v_pk_fma_f16 v173, v173, s20, v199 op_sel_hi:[1,0,0]
	v_pk_fma_f16 v172, v172, s20, v199 op_sel_hi:[1,0,0]
	v_pk_max_f16 v171, v171, v173
	v_pk_max_f16 v170, v170, v172
	s_waitcnt lgkmcnt(5)
	v_mfma_f32_32x32x16_f16 v[34:49], v[74:77], v[234:237], v[34:49]
	ds_read_b128 v[230:233], v179 offset:480
	v_cvt_pk_f16_f32 v30, v30, v31
	v_cvt_pk_f16_f32 v31, v32, v33
	s_waitcnt lgkmcnt(5)
	v_mfma_f32_32x32x16_f16 v[34:49], v[106:109], v[22:25], v[34:49]
	v_exp_f16_e64 v32, v30 clamp
	v_exp_f16_e64 v33, v31 clamp
	v_exp_f16_sdwa v32, v30 clamp dst_sel:WORD_1 dst_unused:UNUSED_PRESERVE src0_sel:WORD_1
	v_exp_f16_sdwa v33, v31 clamp dst_sel:WORD_1 dst_unused:UNUSED_PRESERVE src0_sel:WORD_1
	s_nop 0
	s_waitcnt lgkmcnt(4)
	v_mfma_f32_32x32x16_f16 v[34:49], v[82:85], v[162:165], v[34:49]
	v_pk_fma_f16 v22, v33, s20, v199 op_sel_hi:[1,0,0]
	s_nop 0
	v_pk_max_f16 v173, v31, v22
	v_pk_fma_f16 v22, v32, s20, v199 op_sel_hi:[1,0,0]
	s_nop 0
	v_pk_max_f16 v172, v30, v22
	s_waitcnt lgkmcnt(3)
	v_mfma_f32_32x32x16_f16 v[34:49], v[110:113], v[166:169], v[34:49]
	s_waitcnt vmcnt(1)
	v_pk_add_f16 v24, v146, v154
	v_pk_add_f16 v25, v147, v155
	s_nop 0
	v_pk_mul_f16 v22, v156, v148 clamp
	v_pk_mul_f16 v23, v157, v149 clamp
	v_pk_max_f16 v22, v24, v22
	v_pk_max_f16 v23, v25, v23
	ds_write_b64 v189, v[22:23] offset:33792
	v_mfma_f32_16x16x32_f16 v[62:65], v[66:69], v[170:173], v[62:65]
	s_waitcnt lgkmcnt(3)
	v_mfma_f32_32x32x16_f16 v[34:49], v[94:97], v[26:29], v[34:49]
	v_pk_add_f16 v24, v138, v154
	v_pk_add_f16 v25, v139, v155
	s_nop 0
	v_pk_mul_f16 v22, v156, v140 clamp
	v_pk_mul_f16 v23, v157, v141 clamp
	v_pk_max_f16 v22, v24, v22
	v_pk_max_f16 v23, v25, v23
	ds_write_b64 v189, v[22:23] offset:34320
	s_waitcnt lgkmcnt(3)
	v_mfma_f32_32x32x16_f16 v[34:49], v[134:137], v[18:21], v[34:49]
	v_pk_add_f16 v24, v150, v154
	v_pk_add_f16 v25, v151, v155
	s_nop 0
	v_pk_mul_f16 v22, v156, v152 clamp
	v_pk_mul_f16 v23, v157, v153 clamp
	v_pk_max_f16 v22, v24, v22
	v_pk_max_f16 v23, v25, v23
	ds_write_b64 v189, v[22:23] offset:34848
	s_waitcnt lgkmcnt(3)
	v_mfma_f32_32x32x16_f16 v[34:49], v[130:133], v[230:233], v[34:49]
	v_pk_add_f16 v20, v142, v154
	v_pk_add_f16 v21, v143, v155
	s_nop 0
	v_pk_mul_f16 v18, v156, v144 clamp
	v_pk_mul_f16 v19, v157, v145 clamp
	v_pk_max_f16 v18, v20, v18
	v_pk_max_f16 v19, v21, v19
	ds_write_b64 v189, v[18:19] offset:35376
	ds_write2_b32 v229, v62, v63 offset1:1
	s_and_saveexec_b64 s[20:21], s[0:1]
	ds_write2_b32 v229, v64, v65 offset0:2 offset1:3
	s_or_b64 exec, exec, s[20:21]
	ds_read_b128 v[50:53], v179 offset:16896
	ds_read_b128 v[54:57], v179 offset:16928
	ds_read_b128 v[58:61], v179 offset:16960
	ds_read_b128 v[62:65], v179 offset:16992
	ds_read_b128 v[154:157], v179 offset:17024
	ds_read_b128 v[162:165], v179 offset:17056
	s_waitcnt lgkmcnt(5)
	v_mfma_f32_32x32x16_f16 v[18:33], v[122:125], v[50:53], v[2:17]
	ds_read_b128 v[166:169], v179 offset:17088
	v_cvt_pk_f16_f32 v174, v34, v35
	v_cvt_pk_f16_f32 v175, v36, v37
	s_waitcnt lgkmcnt(5)
	v_mfma_f32_32x32x16_f16 v[18:33], v[98:101], v[54:57], v[18:33]
	ds_read_b128 v[34:37], v179 offset:17120
	v_exp_f16_e64 v50, v174 clamp
	v_exp_f16_e64 v51, v175 clamp
	v_exp_f16_sdwa v50, v174 clamp dst_sel:WORD_1 dst_unused:UNUSED_PRESERVE src0_sel:WORD_1
	v_exp_f16_sdwa v51, v175 clamp dst_sel:WORD_1 dst_unused:UNUSED_PRESERVE src0_sel:WORD_1
	s_nop 0
	s_waitcnt lgkmcnt(5)
	v_mfma_f32_32x32x16_f16 v[18:33], v[114:117], v[58:61], v[18:33]
	ds_read_b128 v[170:173], v179 offset:17152
	s_movk_i32 s20, 0x3dc5
	v_mov_b32_e32 v199, 0xbdc5
	v_pk_fma_f16 v51, v51, s20, v199 op_sel_hi:[1,0,0]
	v_pk_fma_f16 v50, v50, s20, v199 op_sel_hi:[1,0,0]
	v_pk_max_f16 v51, v175, v51
	v_pk_max_f16 v50, v174, v50
	s_waitcnt lgkmcnt(5)
	v_mfma_f32_32x32x16_f16 v[18:33], v[86:89], v[62:65], v[18:33]
	ds_read_b128 v[228:231], v179 offset:17184
	v_cvt_pk_f16_f32 v52, v38, v39
	v_cvt_pk_f16_f32 v53, v40, v41
	s_waitcnt lgkmcnt(5)
	v_mfma_f32_32x32x16_f16 v[18:33], v[126:129], v[154:157], v[18:33]
	ds_read_b128 v[38:41], v179 offset:17216
	v_exp_f16_e64 v54, v52 clamp
	v_exp_f16_e64 v55, v53 clamp
	v_exp_f16_sdwa v54, v52 clamp dst_sel:WORD_1 dst_unused:UNUSED_PRESERVE src0_sel:WORD_1
	v_exp_f16_sdwa v55, v53 clamp dst_sel:WORD_1 dst_unused:UNUSED_PRESERVE src0_sel:WORD_1
	s_nop 0
	s_waitcnt lgkmcnt(5)
	v_mfma_f32_32x32x16_f16 v[18:33], v[90:93], v[162:165], v[18:33]
	ds_read_b128 v[154:157], v179 offset:17248
	v_pk_fma_f16 v55, v55, s20, v199 op_sel_hi:[1,0,0]
	v_pk_fma_f16 v54, v54, s20, v199 op_sel_hi:[1,0,0]
	v_pk_max_f16 v53, v53, v55
	v_pk_max_f16 v52, v52, v54
	s_waitcnt lgkmcnt(5)
	v_mfma_f32_32x32x16_f16 v[18:33], v[118:121], v[166:169], v[18:33]
	ds_read_b128 v[162:165], v179 offset:17280
	v_cvt_pk_f16_f32 v166, v42, v43
	v_cvt_pk_f16_f32 v167, v44, v45
	v_mfma_f32_16x16x32_f16 v[62:65], v[70:73], v[50:53], 0
	s_waitcnt lgkmcnt(5)
	v_mfma_f32_32x32x16_f16 v[18:33], v[78:81], v[34:37], v[18:33]
	ds_read_b128 v[42:45], v179 offset:17312
	v_exp_f16_e64 v168, v166 clamp
	v_exp_f16_e64 v169, v167 clamp
	v_exp_f16_sdwa v168, v166 clamp dst_sel:WORD_1 dst_unused:UNUSED_PRESERVE src0_sel:WORD_1
	v_exp_f16_sdwa v169, v167 clamp dst_sel:WORD_1 dst_unused:UNUSED_PRESERVE src0_sel:WORD_1
	s_nop 0
	s_waitcnt lgkmcnt(5)
	v_mfma_f32_32x32x16_f16 v[18:33], v[102:105], v[170:173], v[18:33]
	ds_read_b128 v[34:37], v179 offset:17344
	v_pk_fma_f16 v169, v169, s20, v199 op_sel_hi:[1,0,0]
	v_pk_fma_f16 v168, v168, s20, v199 op_sel_hi:[1,0,0]
	v_pk_max_f16 v167, v167, v169
	v_pk_max_f16 v166, v166, v168
	s_waitcnt lgkmcnt(5)
	v_mfma_f32_32x32x16_f16 v[18:33], v[74:77], v[228:231], v[18:33]
	ds_read_b128 v[170:173], v179 offset:17376
	v_cvt_pk_f16_f32 v46, v46, v47
	v_cvt_pk_f16_f32 v47, v48, v49
	s_waitcnt lgkmcnt(5)
	v_mfma_f32_32x32x16_f16 v[18:33], v[106:109], v[38:41], v[18:33]
	v_exp_f16_e64 v48, v46 clamp
	v_exp_f16_e64 v49, v47 clamp
	v_exp_f16_sdwa v48, v46 clamp dst_sel:WORD_1 dst_unused:UNUSED_PRESERVE src0_sel:WORD_1
	v_exp_f16_sdwa v49, v47 clamp dst_sel:WORD_1 dst_unused:UNUSED_PRESERVE src0_sel:WORD_1
	s_nop 0
	s_waitcnt lgkmcnt(4)
	v_mfma_f32_32x32x16_f16 v[18:33], v[82:85], v[154:157], v[18:33]
	v_pk_fma_f16 v38, v49, s20, v199 op_sel_hi:[1,0,0]
	s_nop 0
	v_pk_max_f16 v169, v47, v38
	v_pk_fma_f16 v38, v48, s20, v199 op_sel_hi:[1,0,0]
	s_nop 0
	v_pk_max_f16 v168, v46, v38
	s_waitcnt lgkmcnt(3)
	v_mfma_f32_32x32x16_f16 v[18:33], v[110:113], v[162:165], v[18:33]
	s_waitcnt vmcnt(0)
	v_pk_add_f16 v40, v146, v158
	v_pk_add_f16 v41, v147, v159
	s_nop 0
	v_pk_mul_f16 v38, v160, v148 clamp
	v_pk_mul_f16 v39, v161, v149 clamp
	v_pk_max_f16 v38, v40, v38
	v_pk_max_f16 v39, v41, v39
	ds_write_b64 v189, v[38:39] offset:50688
	v_mfma_f32_16x16x32_f16 v[62:65], v[66:69], v[166:169], v[62:65]
	s_waitcnt lgkmcnt(3)
	v_mfma_f32_32x32x16_f16 v[18:33], v[94:97], v[42:45], v[18:33]
	v_pk_add_f16 v40, v138, v158
	v_pk_add_f16 v41, v139, v159
	s_nop 0
	v_pk_mul_f16 v38, v160, v140 clamp
	v_pk_mul_f16 v39, v161, v141 clamp
	v_pk_max_f16 v38, v40, v38
	v_pk_max_f16 v39, v41, v39
	ds_write_b64 v189, v[38:39] offset:51216
	s_waitcnt lgkmcnt(3)
	v_mfma_f32_32x32x16_f16 v[18:33], v[134:137], v[34:37], v[18:33]
	v_pk_add_f16 v40, v150, v158
	v_pk_add_f16 v41, v151, v159
	s_nop 0
	v_pk_mul_f16 v38, v160, v152 clamp
	v_pk_mul_f16 v39, v161, v153 clamp
	v_pk_max_f16 v38, v40, v38
	v_pk_max_f16 v39, v41, v39
	ds_write_b64 v189, v[38:39] offset:51744
	s_waitcnt lgkmcnt(3)
	v_mfma_f32_32x32x16_f16 v[18:33], v[130:133], v[170:173], v[18:33]
	v_pk_add_f16 v36, v142, v158
	v_pk_add_f16 v37, v143, v159
	s_nop 0
	v_pk_mul_f16 v34, v160, v144 clamp
	v_pk_mul_f16 v35, v161, v145 clamp
	v_pk_max_f16 v34, v36, v34
	v_pk_max_f16 v35, v37, v35
	ds_write_b64 v189, v[34:35] offset:52272
	ds_write2_b32 v206, v62, v63 offset1:1
	s_and_saveexec_b64 s[20:21], s[0:1]
	ds_write2_b32 v206, v64, v65 offset0:2 offset1:3
	s_or_b64 exec, exec, s[20:21]
	s_sub_i32 s20, 0x7c, s30
	s_mul_i32 s20, s20, 6
	s_ashr_i32 s21, s20, 31
	s_add_u32 s12, s12, s20
	s_addc_u32 s13, s13, s21
	s_and_b64 vcc, exec, s[8:9]
	s_waitcnt lgkmcnt(0)
	s_barrier
	s_cbranch_vccnz .LBB1_190
	s_cmp_lg_u32 s41, 0
	s_cbranch_scc0 .LBB1_186
	s_and_saveexec_b64 s[20:21], s[6:7]
	s_cbranch_execz .LBB1_185
	ds_read2_b32 v[34:35], v180 offset1:224
	v_add_u32_e32 v36, 0x700, v180
	v_add_u32_e32 v38, 0xe00, v180
	ds_read2_b32 v[36:37], v36 offset1:224
	ds_read2_b32 v[38:39], v38 offset1:224
	s_waitcnt lgkmcnt(2)
	v_add_f32_e32 v34, 0, v34
	v_add_f32_e32 v40, v34, v35
	v_add_u32_e32 v34, 0x1500, v180
	ds_read2_b32 v[34:35], v34 offset1:224
	s_waitcnt lgkmcnt(2)
	v_add_f32_e32 v36, v40, v36
	v_add_f32_e32 v36, v36, v37
	s_waitcnt lgkmcnt(1)
	v_add_f32_e32 v36, v36, v38
	v_add_f32_e32 v36, v36, v39
	s_waitcnt lgkmcnt(0)
	v_add_f32_e32 v34, v36, v34
	v_add_f32_e32 v34, v34, v35
	v_mov_b32_e32 v35, 0x19180
	v_lshl_add_u32 v35, v177, 2, v35
	ds_write_b32 v35, v34
